# v4 bundle + GEMM stage-DMA rebalance (5 instances) + router matrix LDS staging with 16 loads in flight
# baseline (speedup 1.0000x reference)
; #define PG8_STAGE(bufoff, gbase, voff) do { _Pragma("unroll") for (int _i = 0; _i < 2; ++_i) \
;         __builtin_amdgcn_global_load_lds((const unsigned*)((const char*)(gbase) + (voff)[_i]), (PG8_LAS unsigned*)(lds + (bufoff) + ldsw + _i * 8192), 16, 0, 0); } while (0)
; #define PG8_LDA(dst, b, h) do { _Pragma("unroll") for (int m = 0; m < 4; ++m) _Pragma("unroll") for (int k = 0; k < 2; ++k) dst[m][k] = *(const PG8_LAS bf16x8*)(lds + PG8_SA(b, h) + aoff + m * 2048 + k * 1024); } while (0)
; #define PG8_LDB(dst, b, h) do { _Pragma("unroll") for (int n = 0; n < 2; ++n) _Pragma("unroll") for (int k = 0; k < 2; ++k) dst[n][k] = *(const PG8_LAS bf16x8*)(lds + PG8_SB(b, h) + boff + n * 2048 + k * 1024); } while (0)
; #define PG8_WAIT_V(n) asm volatile("s_waitcnt vmcnt(" #n ")" ::: "memory")
; #define PG8_WAIT_L(n) asm volatile("s_waitcnt lgkmcnt(" #n ")" ::: "memory")
; #define PG8_BAR __builtin_amdgcn_s_barrier()
; template <class Epi, class Sched, bool ALIGN_EPI = false, bool SP2 = false, bool GATHER = false>
; __device__ __forceinline__ void gemm_phase(PG8_LAS unsigned char* lds, const Gemm g, const Sched& S, const Epi& E, int tid_in, const int* rowsrc = nullptr, PG8_LAS int* idx_lds = nullptr) {
;     ...
;         for (int t = 0; t < nt; t += 2) {
;             const bool last = (t == nt - 2);
;             if constexpr (GATHER) {
; #pragma unroll
;                 for (int h_ = 0; h_ < 2; ++h_) { gS[h_][0] = last ? gN[h_][0] : gA[h_][0]; gS[h_][1] = last ? gN[h_][1] : gA[h_][1]; } }
;             const char* a1 = cA + (size_t)(t + 1) * kstep;
;             const char* a2 = last ? nA : cA + (size_t)(t + 2) * kstep; const char* b2 = last ? nB : cB + (size_t)(t + 2) * kstep;
;             const char* a3 = a2 + kstep; const char* b3 = b2 + kstep;
;             if (last && has_next) S.a_ready(nxt);
;             if constexpr (SP2) {
;             PG8_LDB(B0, 0, 0); PG8_LDB(B1, 0, 1); PG8_SCHED; PG8_LDA(At, 0, 0); PG8_STAGE(PG8_SA(1, 1), a1 + hstepA, PG8_OA(1));
;             PG8_WAIT_V(8); PG8_WAIT_L(0); PG8_BAR; PG8_MMA(0, 0, At, B0); PG8_MMA(0, 1, At, B1); PG8_BAR; PG8_SCHED;
;             PG8_LDA(At, 0, 1); PG8_STAGE(PG8_SB(0, 0), b2, voffB); PG8_STAGE(PG8_SB(0, 1), b2 + hstep, voffB); PG8_STAGE(PG8_SA(0, 0), a2, PG8_OS(0));
;             PG8_WAIT_V(8); PG8_WAIT_L(0); PG8_BAR; PG8_MMA(1, 0, At, B0); PG8_MMA(1, 1, At, B1); PG8_BAR; PG8_SCHED;
.LBB0_390:
	s_add_u32 s20, s18, 0xfffc0080
	s_addc_u32 s21, s19, -1
	s_add_i32 s52, 0, 0x10000
	s_cmp_eq_u32 s51, 12
	s_cselect_b32 s23, s13, s21
	s_cselect_b32 s22, s47, s20
	v_add_u32_e32 v144, s52, v149
	s_cselect_b32 s21, s9, s50
	s_cselect_b32 s20, s48, s49
	s_add_i32 s54, 0, 0x14000
	ds_read_b128 v[140:143], v144
	ds_read_b128 v[152:155], v144 offset:1024
	ds_read_b128 v[156:159], v144 offset:2048
	ds_read_b128 v[160:163], v144 offset:3072
	v_add_u32_e32 v144, s54, v149
	ds_read_b128 v[164:167], v144
	ds_read_b128 v[168:171], v144 offset:1024
	ds_read_b128 v[172:175], v144 offset:2048
	ds_read_b128 v[176:179], v144 offset:3072
	v_lshl_add_u64 v[144:145], s[18:19], 0, v[136:137]
	s_add_i32 m0, s29, 0xc000
	ds_read_b128 v[180:183], v151
	ds_read_b128 v[184:187], v151 offset:1024
	ds_read_b128 v[188:191], v151 offset:2048
	ds_read_b128 v[192:195], v151 offset:3072
	ds_read_b128 v[196:199], v151 offset:4096
	ds_read_b128 v[200:203], v151 offset:5120
	ds_read_b128 v[204:207], v151 offset:6144
	ds_read_b128 v[208:211], v151 offset:7168
	global_load_lds_dwordx4 v[144:145], off
	v_lshl_add_u64 v[144:145], s[18:19], 0, v[138:139]
	s_add_i32 m0, s29, 0xe000
	s_nop 0
	global_load_lds_dwordx4 v[144:145], off
	s_waitcnt vmcnt(8)
	s_waitcnt lgkmcnt(0)
	v_mfma_f32_16x16x32_bf16 v[126:129], v[140:143], v[180:183], v[126:129]
	v_mfma_f32_16x16x32_bf16 v[122:125], v[156:159], v[180:183], v[122:125]
	v_mfma_f32_16x16x32_bf16 v[110:113], v[140:143], v[188:191], v[110:113]
	s_barrier
	s_setprio 1
	s_waitcnt lgkmcnt(0)
	v_mfma_f32_16x16x32_bf16 v[106:109], v[156:159], v[188:191], v[106:109]
	v_mfma_f32_16x16x32_bf16 v[94:97], v[140:143], v[196:199], v[94:97]
	v_mfma_f32_16x16x32_bf16 v[90:93], v[156:159], v[196:199], v[90:93]
	v_mfma_f32_16x16x32_bf16 v[78:81], v[140:143], v[204:207], v[78:81]
	v_mfma_f32_16x16x32_bf16 v[74:77], v[156:159], v[204:207], v[74:77]
	v_mfma_f32_16x16x32_bf16 v[126:129], v[152:155], v[184:187], v[126:129]
	v_mfma_f32_16x16x32_bf16 v[122:125], v[160:163], v[184:187], v[122:125]
	v_mfma_f32_16x16x32_bf16 v[110:113], v[152:155], v[192:195], v[110:113]
	v_mfma_f32_16x16x32_bf16 v[106:109], v[160:163], v[192:195], v[106:109]
	v_mfma_f32_16x16x32_bf16 v[94:97], v[152:155], v[200:203], v[94:97]
	v_mfma_f32_16x16x32_bf16 v[90:93], v[160:163], v[200:203], v[90:93]
	v_mfma_f32_16x16x32_bf16 v[78:81], v[152:155], v[208:211], v[78:81]
	v_mfma_f32_16x16x32_bf16 v[74:77], v[160:163], v[208:211], v[74:77]
	s_setprio 0
	s_setprio 1
	v_mfma_f32_16x16x32_bf16 v[118:121], v[164:167], v[180:183], v[118:121]
	v_mfma_f32_16x16x32_bf16 v[114:117], v[172:175], v[180:183], v[114:117]
	v_mfma_f32_16x16x32_bf16 v[102:105], v[164:167], v[188:191], v[102:105]
	v_mfma_f32_16x16x32_bf16 v[98:101], v[172:175], v[188:191], v[98:101]
	v_mfma_f32_16x16x32_bf16 v[86:89], v[164:167], v[196:199], v[86:89]
	v_mfma_f32_16x16x32_bf16 v[82:85], v[172:175], v[196:199], v[82:85]
	v_mfma_f32_16x16x32_bf16 v[70:73], v[164:167], v[204:207], v[70:73]
	v_mfma_f32_16x16x32_bf16 v[66:69], v[172:175], v[204:207], v[66:69]
	v_mfma_f32_16x16x32_bf16 v[118:121], v[168:171], v[184:187], v[118:121]
	v_mfma_f32_16x16x32_bf16 v[114:117], v[176:179], v[184:187], v[114:117]
	v_mfma_f32_16x16x32_bf16 v[102:105], v[168:171], v[192:195], v[102:105]
	v_mfma_f32_16x16x32_bf16 v[98:101], v[176:179], v[192:195], v[98:101]
	v_mfma_f32_16x16x32_bf16 v[86:89], v[168:171], v[200:203], v[86:89]
	v_mfma_f32_16x16x32_bf16 v[82:85], v[176:179], v[200:203], v[82:85]
	v_mfma_f32_16x16x32_bf16 v[70:73], v[168:171], v[208:211], v[70:73]
	v_mfma_f32_16x16x32_bf16 v[66:69], v[176:179], v[208:211], v[66:69]
	s_setprio 0
	s_barrier
	s_add_i32 s52, s52, s28
	v_lshl_add_u64 v[144:145], s[20:21], 0, v[0:1]
	s_mov_b32 m0, s52
	ds_read_b128 v[180:183], v151 offset:16384
	ds_read_b128 v[184:187], v151 offset:17408
	ds_read_b128 v[188:191], v151 offset:18432
	ds_read_b128 v[192:195], v151 offset:19456
	ds_read_b128 v[196:199], v151 offset:20480
	ds_read_b128 v[200:203], v151 offset:21504
	ds_read_b128 v[204:207], v151 offset:22528
	ds_read_b128 v[208:211], v151 offset:23552
	global_load_lds_dwordx4 v[144:145], off
	s_add_i32 m0, s52, 0x2000
	s_add_u32 s52, s20, 0x40000
	v_lshl_add_u64 v[212:213], s[20:21], 0, v[130:131]
	s_addc_u32 s53, s21, 0
	s_add_i32 s54, s54, s28
	global_load_lds_dwordx4 v[212:213], off
	v_lshl_add_u64 v[214:215], s[52:53], 0, v[0:1]
	s_mov_b32 m0, s54
	v_lshl_add_u64 v[216:217], s[22:23], 0, v[132:133]
	global_load_lds_dwordx4 v[214:215], off
	s_waitcnt vmcnt(5)
	s_waitcnt lgkmcnt(0)
	v_mfma_f32_16x16x32_bf16 v[62:65], v[140:143], v[180:183], v[62:65]
	v_mfma_f32_16x16x32_bf16 v[58:61], v[156:159], v[180:183], v[58:61]
	v_mfma_f32_16x16x32_bf16 v[46:49], v[140:143], v[188:191], v[46:49]
	s_barrier
; #define PG8_STAGE(bufoff, gbase, voff) do { _Pragma("unroll") for (int _i = 0; _i < 2; ++_i) \
;         __builtin_amdgcn_global_load_lds((const unsigned*)((const char*)(gbase) + (voff)[_i]), (PG8_LAS unsigned*)(lds + (bufoff) + ldsw + _i * 8192), 16, 0, 0); } while (0)
; #define PG8_LDA(dst, b, h) do { _Pragma("unroll") for (int m = 0; m < 4; ++m) _Pragma("unroll") for (int k = 0; k < 2; ++k) dst[m][k] = *(const PG8_LAS bf16x8*)(lds + PG8_SA(b, h) + aoff + m * 2048 + k * 1024); } while (0)
; #define PG8_LDB(dst, b, h) do { _Pragma("unroll") for (int n = 0; n < 2; ++n) _Pragma("unroll") for (int k = 0; k < 2; ++k) dst[n][k] = *(const PG8_LAS bf16x8*)(lds + PG8_SB(b, h) + boff + n * 2048 + k * 1024); } while (0)
; #define PG8_MMA(ai, bj, At, Bt) do { __builtin_amdgcn_s_setprio(1); _Pragma("unroll") for (int m = 0; m < 4; ++m) _Pragma("unroll") for (int n = 0; n < 2; ++n) _Pragma("unroll") for (int k = 0; k < 2; ++k) \
;         acc[ai][bj][m][n] = __builtin_amdgcn_mfma_f32_16x16x32_bf16(Bt[n][k], At[m][k], acc[ai][bj][m][n], 0, 0, 0); __builtin_amdgcn_s_setprio(0); } while (0)
; #define PG8_WAIT_V(n) asm volatile("s_waitcnt vmcnt(" #n ")" ::: "memory")
; #define PG8_WAIT_L(n) asm volatile("s_waitcnt lgkmcnt(" #n ")" ::: "memory")
; #define PG8_BAR __builtin_amdgcn_s_barrier()
; #define PG8_SCHED __builtin_amdgcn_sched_barrier(0)
; template <class Epi, class Sched, bool ALIGN_EPI = false, bool SP2 = false, bool GATHER = false>
; __device__ __forceinline__ void gemm_phase(PG8_LAS unsigned char* lds, const Gemm g, const Sched& S, const Epi& E, int tid_in, const int* rowsrc = nullptr, PG8_LAS int* idx_lds = nullptr) {
;     ...
;             PG8_WAIT_V(8); PG8_WAIT_L(0); PG8_BAR; PG8_MMA(1, 0, At, B0); PG8_MMA(1, 1, At, B1); PG8_BAR; PG8_SCHED;
;             PG8_LDB(B0, 1, 0); PG8_LDB(B1, 1, 1); PG8_SCHED; PG8_LDA(At, 1, 0); PG8_STAGE(PG8_SA(0, 1), a2 + hstepA, PG8_OS(1));
;             PG8_WAIT_V(8); PG8_WAIT_L(0); PG8_BAR; PG8_MMA(0, 0, At, B0); PG8_MMA(0, 1, At, B1); PG8_BAR; PG8_SCHED;
	s_setprio 1
	s_waitcnt lgkmcnt(0)
	v_mfma_f32_16x16x32_bf16 v[42:45], v[156:159], v[188:191], v[42:45]
	v_mfma_f32_16x16x32_bf16 v[30:33], v[140:143], v[196:199], v[30:33]
	v_mfma_f32_16x16x32_bf16 v[26:29], v[156:159], v[196:199], v[26:29]
	v_mfma_f32_16x16x32_bf16 v[14:17], v[140:143], v[204:207], v[14:17]
	v_mfma_f32_16x16x32_bf16 v[10:13], v[156:159], v[204:207], v[10:13]
	v_lshl_add_u64 v[214:215], s[52:53], 0, v[130:131]
	s_add_i32 m0, s54, 0x2000
	s_nop 0
	global_load_lds_dwordx4 v[214:215], off
	v_mfma_f32_16x16x32_bf16 v[62:65], v[152:155], v[184:187], v[62:65]
	v_mfma_f32_16x16x32_bf16 v[58:61], v[160:163], v[184:187], v[58:61]
	v_mfma_f32_16x16x32_bf16 v[46:49], v[152:155], v[192:195], v[46:49]
	v_mfma_f32_16x16x32_bf16 v[42:45], v[160:163], v[192:195], v[42:45]
	v_mfma_f32_16x16x32_bf16 v[30:33], v[152:155], v[200:203], v[30:33]
	v_mfma_f32_16x16x32_bf16 v[26:29], v[160:163], v[200:203], v[26:29]
	v_mfma_f32_16x16x32_bf16 v[14:17], v[152:155], v[208:211], v[14:17]
	v_mfma_f32_16x16x32_bf16 v[10:13], v[160:163], v[208:211], v[10:13]
	v_lshl_add_u64 v[214:215], s[22:23], 0, v[134:135]
	s_mov_b32 m0, s29
	s_nop 0
	global_load_lds_dwordx4 v[214:215], off
	s_setprio 0
	s_setprio 1
	v_mfma_f32_16x16x32_bf16 v[54:57], v[164:167], v[180:183], v[54:57]
	v_mfma_f32_16x16x32_bf16 v[50:53], v[172:175], v[180:183], v[50:53]
	v_mfma_f32_16x16x32_bf16 v[38:41], v[164:167], v[188:191], v[38:41]
	v_mfma_f32_16x16x32_bf16 v[34:37], v[172:175], v[188:191], v[34:37]
	v_mfma_f32_16x16x32_bf16 v[22:25], v[164:167], v[196:199], v[22:25]
	v_mfma_f32_16x16x32_bf16 v[18:21], v[172:175], v[196:199], v[18:21]
	v_mfma_f32_16x16x32_bf16 v[6:9], v[164:167], v[204:207], v[6:9]
	v_mfma_f32_16x16x32_bf16 v[2:5], v[172:175], v[204:207], v[2:5]
	s_mov_b32 m0, s30
	s_nop 0
	global_load_lds_dwordx4 v[216:217], off
	v_mfma_f32_16x16x32_bf16 v[54:57], v[168:171], v[184:187], v[54:57]
	v_mfma_f32_16x16x32_bf16 v[50:53], v[176:179], v[184:187], v[50:53]
	v_mfma_f32_16x16x32_bf16 v[38:41], v[168:171], v[192:195], v[38:41]
	v_mfma_f32_16x16x32_bf16 v[34:37], v[176:179], v[192:195], v[34:37]
	v_mfma_f32_16x16x32_bf16 v[22:25], v[168:171], v[200:203], v[22:25]
	v_mfma_f32_16x16x32_bf16 v[18:21], v[176:179], v[200:203], v[18:21]
	v_mfma_f32_16x16x32_bf16 v[6:9], v[168:171], v[208:211], v[6:9]
	v_mfma_f32_16x16x32_bf16 v[2:5], v[176:179], v[208:211], v[2:5]
	s_setprio 0
	s_barrier
	s_add_i32 s52, 0, 0x18000
	s_add_i32 s53, 0, 0x1c000
	v_add_u32_e32 v160, s52, v149
	v_add_u32_e32 v176, s53, v149
	ds_read_b128 v[140:143], v160
	ds_read_b128 v[152:155], v160 offset:1024
	ds_read_b128 v[156:159], v160 offset:2048
	ds_read_b128 v[160:163], v160 offset:3072
	ds_read_b128 v[164:167], v176
	ds_read_b128 v[168:171], v176 offset:1024
	ds_read_b128 v[172:175], v176 offset:2048
	ds_read_b128 v[176:179], v176 offset:3072
	s_add_u32 s22, s22, 0x40000
	s_addc_u32 s23, s23, 0
	s_mov_b32 m0, s31
	v_lshl_add_u64 v[218:219], s[22:23], 0, v[134:135]
	ds_read_b128 v[180:183], v151 offset:32768
	ds_read_b128 v[184:187], v151 offset:33792
	ds_read_b128 v[188:191], v151 offset:34816
	ds_read_b128 v[192:195], v151 offset:35840
	ds_read_b128 v[196:199], v151 offset:36864
	ds_read_b128 v[200:203], v151 offset:37888
	ds_read_b128 v[204:207], v151 offset:38912
	ds_read_b128 v[208:211], v151 offset:39936
	global_load_lds_dwordx4 v[218:219], off
	v_lshl_add_u64 v[218:219], s[22:23], 0, v[132:133]
	s_mov_b32 m0, s36
	s_nop 0
	global_load_lds_dwordx4 v[218:219], off
	s_waitcnt vmcnt(8)
	s_waitcnt lgkmcnt(0)
	v_mfma_f32_16x16x32_bf16 v[126:129], v[140:143], v[180:183], v[126:129]
	v_mfma_f32_16x16x32_bf16 v[122:125], v[156:159], v[180:183], v[122:125]
	v_mfma_f32_16x16x32_bf16 v[110:113], v[140:143], v[188:191], v[110:113]
	s_barrier
	s_setprio 1
	s_waitcnt lgkmcnt(0)
	v_mfma_f32_16x16x32_bf16 v[106:109], v[156:159], v[188:191], v[106:109]
	v_mfma_f32_16x16x32_bf16 v[94:97], v[140:143], v[196:199], v[94:97]
	v_mfma_f32_16x16x32_bf16 v[90:93], v[156:159], v[196:199], v[90:93]
	v_mfma_f32_16x16x32_bf16 v[78:81], v[140:143], v[204:207], v[78:81]
	v_mfma_f32_16x16x32_bf16 v[74:77], v[156:159], v[204:207], v[74:77]
	v_mfma_f32_16x16x32_bf16 v[126:129], v[152:155], v[184:187], v[126:129]
	v_mfma_f32_16x16x32_bf16 v[122:125], v[160:163], v[184:187], v[122:125]
	v_mfma_f32_16x16x32_bf16 v[110:113], v[152:155], v[192:195], v[110:113]
	v_mfma_f32_16x16x32_bf16 v[106:109], v[160:163], v[192:195], v[106:109]
	v_mfma_f32_16x16x32_bf16 v[94:97], v[152:155], v[200:203], v[94:97]
	v_mfma_f32_16x16x32_bf16 v[90:93], v[160:163], v[200:203], v[90:93]
	v_mfma_f32_16x16x32_bf16 v[78:81], v[152:155], v[208:211], v[78:81]
	v_mfma_f32_16x16x32_bf16 v[74:77], v[160:163], v[208:211], v[74:77]
	s_setprio 0
	s_setprio 1
	v_mfma_f32_16x16x32_bf16 v[118:121], v[164:167], v[180:183], v[118:121]
	v_mfma_f32_16x16x32_bf16 v[114:117], v[172:175], v[180:183], v[114:117]
	v_mfma_f32_16x16x32_bf16 v[102:105], v[164:167], v[188:191], v[102:105]
	v_mfma_f32_16x16x32_bf16 v[98:101], v[172:175], v[188:191], v[98:101]
	v_mfma_f32_16x16x32_bf16 v[86:89], v[164:167], v[196:199], v[86:89]
	v_mfma_f32_16x16x32_bf16 v[82:85], v[172:175], v[196:199], v[82:85]
	v_mfma_f32_16x16x32_bf16 v[70:73], v[164:167], v[204:207], v[70:73]
	v_mfma_f32_16x16x32_bf16 v[66:69], v[172:175], v[204:207], v[66:69]
	v_mfma_f32_16x16x32_bf16 v[118:121], v[168:171], v[184:187], v[118:121]
	v_mfma_f32_16x16x32_bf16 v[114:117], v[176:179], v[184:187], v[114:117]
	v_mfma_f32_16x16x32_bf16 v[102:105], v[168:171], v[192:195], v[102:105]
	v_mfma_f32_16x16x32_bf16 v[98:101], v[176:179], v[192:195], v[98:101]
	v_mfma_f32_16x16x32_bf16 v[86:89], v[168:171], v[200:203], v[86:89]
	v_mfma_f32_16x16x32_bf16 v[82:85], v[176:179], v[200:203], v[82:85]
	v_mfma_f32_16x16x32_bf16 v[70:73], v[168:171], v[208:211], v[70:73]
	v_mfma_f32_16x16x32_bf16 v[66:69], v[176:179], v[208:211], v[66:69]
	s_setprio 0
	s_barrier
; #define PG8_STAGE(bufoff, gbase, voff) do { _Pragma("unroll") for (int _i = 0; _i < 2; ++_i) \
;         __builtin_amdgcn_global_load_lds((const unsigned*)((const char*)(gbase) + (voff)[_i]), (PG8_LAS unsigned*)(lds + (bufoff) + ldsw + _i * 8192), 16, 0, 0); } while (0)
; #define PG8_LDA(dst, b, h) do { _Pragma("unroll") for (int m = 0; m < 4; ++m) _Pragma("unroll") for (int k = 0; k < 2; ++k) dst[m][k] = *(const PG8_LAS bf16x8*)(lds + PG8_SA(b, h) + aoff + m * 2048 + k * 1024); } while (0)
; #define PG8_MMA(ai, bj, At, Bt) do { __builtin_amdgcn_s_setprio(1); _Pragma("unroll") for (int m = 0; m < 4; ++m) _Pragma("unroll") for (int n = 0; n < 2; ++n) _Pragma("unroll") for (int k = 0; k < 2; ++k) \
;         acc[ai][bj][m][n] = __builtin_amdgcn_mfma_f32_16x16x32_bf16(Bt[n][k], At[m][k], acc[ai][bj][m][n], 0, 0, 0); __builtin_amdgcn_s_setprio(0); } while (0)
; #define PG8_WAIT_V(n) asm volatile("s_waitcnt vmcnt(" #n ")" ::: "memory")
; #define PG8_WAIT_L(n) asm volatile("s_waitcnt lgkmcnt(" #n ")" ::: "memory")
; #define PG8_BAR __builtin_amdgcn_s_barrier()
; #define PG8_SCHED __builtin_amdgcn_sched_barrier(0)
; template <class Epi, class Sched, bool ALIGN_EPI = false, bool SP2 = false, bool GATHER = false>
; __device__ __forceinline__ void gemm_phase(PG8_LAS unsigned char* lds, const Gemm g, const Sched& S, const Epi& E, int tid_in, const int* rowsrc = nullptr, PG8_LAS int* idx_lds = nullptr) {
;     ...
;             PG8_LDA(At, 1, 1); PG8_STAGE(PG8_SB(1, 0), b3, voffB); PG8_STAGE(PG8_SB(1, 1), b3 + hstep, voffB); PG8_STAGE(PG8_SA(1, 0), a3, PG8_OS(0));
;             PG8_WAIT_V(8); PG8_WAIT_L(0); PG8_BAR; PG8_MMA(1, 0, At, B0); PG8_MMA(1, 1, At, B1); PG8_BAR; PG8_SCHED;
;     ...
;         if constexpr (ALIGN_EPI) { if (wr == 0) PG8_BAR; }
	s_add_i32 s22, s52, s28
	v_lshl_add_u64 v[144:145], v[144:145], 0, s[10:11]
	s_mov_b32 m0, s22
	ds_read_b128 v[180:183], v151 offset:49152
	ds_read_b128 v[184:187], v151 offset:50176
	ds_read_b128 v[188:191], v151 offset:51200
	ds_read_b128 v[192:195], v151 offset:52224
	ds_read_b128 v[196:199], v151 offset:53248
	ds_read_b128 v[200:203], v151 offset:54272
	ds_read_b128 v[204:207], v151 offset:55296
	ds_read_b128 v[208:211], v151 offset:56320
	global_load_lds_dwordx4 v[144:145], off
	s_add_i32 m0, s22, 0x2000
	s_add_u32 s20, s20, 0x40080
	v_lshl_add_u64 v[144:145], v[212:213], 0, s[10:11]
	s_addc_u32 s21, s21, 0
	s_add_i32 s22, s53, s28
	global_load_lds_dwordx4 v[144:145], off
	v_lshl_add_u64 v[144:145], s[20:21], 0, v[0:1]
	s_mov_b32 m0, s22
	s_nop 0
	global_load_lds_dwordx4 v[144:145], off
	s_waitcnt vmcnt(5)
	s_waitcnt lgkmcnt(0)
	v_mfma_f32_16x16x32_bf16 v[62:65], v[140:143], v[180:183], v[62:65]
	v_mfma_f32_16x16x32_bf16 v[58:61], v[156:159], v[180:183], v[58:61]
	v_mfma_f32_16x16x32_bf16 v[46:49], v[140:143], v[188:191], v[46:49]
	s_barrier
	s_setprio 1
	s_waitcnt lgkmcnt(0)
	v_mfma_f32_16x16x32_bf16 v[42:45], v[156:159], v[188:191], v[42:45]
	v_mfma_f32_16x16x32_bf16 v[30:33], v[140:143], v[196:199], v[30:33]
	v_mfma_f32_16x16x32_bf16 v[26:29], v[156:159], v[196:199], v[26:29]
	v_mfma_f32_16x16x32_bf16 v[14:17], v[140:143], v[204:207], v[14:17]
	v_mfma_f32_16x16x32_bf16 v[10:13], v[156:159], v[204:207], v[10:13]
	v_lshl_add_u64 v[144:145], s[20:21], 0, v[130:131]
	s_add_i32 m0, s22, 0x2000
	s_nop 0
	global_load_lds_dwordx4 v[144:145], off
	v_mfma_f32_16x16x32_bf16 v[62:65], v[152:155], v[184:187], v[62:65]
	v_mfma_f32_16x16x32_bf16 v[58:61], v[160:163], v[184:187], v[58:61]
	v_mfma_f32_16x16x32_bf16 v[46:49], v[152:155], v[192:195], v[46:49]
	v_mfma_f32_16x16x32_bf16 v[42:45], v[160:163], v[192:195], v[42:45]
	v_mfma_f32_16x16x32_bf16 v[30:33], v[152:155], v[200:203], v[30:33]
	v_mfma_f32_16x16x32_bf16 v[26:29], v[160:163], v[200:203], v[26:29]
	v_mfma_f32_16x16x32_bf16 v[14:17], v[152:155], v[208:211], v[14:17]
	v_mfma_f32_16x16x32_bf16 v[10:13], v[160:163], v[208:211], v[10:13]
	v_lshl_add_u64 v[144:145], v[214:215], 0, s[10:11]
	s_mov_b32 m0, s38
	s_nop 0
	global_load_lds_dwordx4 v[144:145], off
	s_setprio 0
	s_setprio 1
	v_mfma_f32_16x16x32_bf16 v[54:57], v[164:167], v[180:183], v[54:57]
	v_mfma_f32_16x16x32_bf16 v[50:53], v[172:175], v[180:183], v[50:53]
	v_mfma_f32_16x16x32_bf16 v[38:41], v[164:167], v[188:191], v[38:41]
	v_mfma_f32_16x16x32_bf16 v[34:37], v[172:175], v[188:191], v[34:37]
	v_mfma_f32_16x16x32_bf16 v[22:25], v[164:167], v[196:199], v[22:25]
	v_mfma_f32_16x16x32_bf16 v[18:21], v[172:175], v[196:199], v[18:21]
	v_mfma_f32_16x16x32_bf16 v[6:9], v[164:167], v[204:207], v[6:9]
	v_mfma_f32_16x16x32_bf16 v[2:5], v[172:175], v[204:207], v[2:5]
	v_lshl_add_u64 v[144:145], v[216:217], 0, s[10:11]
	s_mov_b32 m0, s39
	s_nop 0
	global_load_lds_dwordx4 v[144:145], off
	v_mfma_f32_16x16x32_bf16 v[54:57], v[168:171], v[184:187], v[54:57]
	v_mfma_f32_16x16x32_bf16 v[50:53], v[176:179], v[184:187], v[50:53]
	v_mfma_f32_16x16x32_bf16 v[38:41], v[168:171], v[192:195], v[38:41]
	v_mfma_f32_16x16x32_bf16 v[34:37], v[176:179], v[192:195], v[34:37]
	v_mfma_f32_16x16x32_bf16 v[22:25], v[168:171], v[200:203], v[22:25]
	v_mfma_f32_16x16x32_bf16 v[18:21], v[176:179], v[200:203], v[18:21]
	v_mfma_f32_16x16x32_bf16 v[6:9], v[168:171], v[208:211], v[6:9]
	v_mfma_f32_16x16x32_bf16 v[2:5], v[176:179], v[208:211], v[2:5]
	s_setprio 0
	s_barrier
	s_add_i32 s51, s51, 2
	s_add_u32 s18, s18, 0x100
	s_addc_u32 s19, s19, 0
	s_add_u32 s49, s49, 0x100
	s_addc_u32 s50, s50, 0
	s_cmp_gt_u32 s51, 13
	s_cbranch_scc0 .LBB0_390
	s_and_b64 vcc, exec, s[6:7]
	s_cbranch_vccz .LBB0_393
	s_barrier

; #define PG8_STAGE(bufoff, gbase, voff) do { _Pragma("unroll") for (int _i = 0; _i < 2; ++_i) \
;         __builtin_amdgcn_global_load_lds((const unsigned*)((const char*)(gbase) + (voff)[_i]), (PG8_LAS unsigned*)(lds + (bufoff) + ldsw + _i * 8192), 16, 0, 0); } while (0)
; #define PG8_LDA(dst, b, h) do { _Pragma("unroll") for (int m = 0; m < 4; ++m) _Pragma("unroll") for (int k = 0; k < 2; ++k) dst[m][k] = *(const PG8_LAS bf16x8*)(lds + PG8_SA(b, h) + aoff + m * 2048 + k * 1024); } while (0)
; #define PG8_LDB(dst, b, h) do { _Pragma("unroll") for (int n = 0; n < 2; ++n) _Pragma("unroll") for (int k = 0; k < 2; ++k) dst[n][k] = *(const PG8_LAS bf16x8*)(lds + PG8_SB(b, h) + boff + n * 2048 + k * 1024); } while (0)
; #define PG8_WAIT_V(n) asm volatile("s_waitcnt vmcnt(" #n ")" ::: "memory")
; #define PG8_WAIT_L(n) asm volatile("s_waitcnt lgkmcnt(" #n ")" ::: "memory")
; #define PG8_BAR __builtin_amdgcn_s_barrier()
; template <class Epi, class Sched, bool ALIGN_EPI = false, bool SP2 = false, bool GATHER = false>
; __device__ __forceinline__ void gemm_phase(PG8_LAS unsigned char* lds, const Gemm g, const Sched& S, const Epi& E, int tid_in, const int* rowsrc = nullptr, PG8_LAS int* idx_lds = nullptr) {
;     ...
;         for (int t = 0; t < nt; t += 2) {
;             const bool last = (t == nt - 2);
;             if constexpr (GATHER) {
; #pragma unroll
;                 for (int h_ = 0; h_ < 2; ++h_) { gS[h_][0] = last ? gN[h_][0] : gA[h_][0]; gS[h_][1] = last ? gN[h_][1] : gA[h_][1]; } }
;             const char* a1 = cA + (size_t)(t + 1) * kstep;
;             const char* a2 = last ? nA : cA + (size_t)(t + 2) * kstep; const char* b2 = last ? nB : cB + (size_t)(t + 2) * kstep;
;             const char* a3 = a2 + kstep; const char* b3 = b2 + kstep;
;             if (last && has_next) S.a_ready(nxt);
;             if constexpr (SP2) {
;             PG8_LDB(B0, 0, 0); PG8_LDB(B1, 0, 1); PG8_SCHED; PG8_LDA(At, 0, 0); PG8_STAGE(PG8_SA(1, 1), a1 + hstepA, PG8_OA(1));
;             PG8_WAIT_V(8); PG8_WAIT_L(0); PG8_BAR; PG8_MMA(0, 0, At, B0); PG8_MMA(0, 1, At, B1); PG8_BAR; PG8_SCHED;
;             PG8_LDA(At, 0, 1); PG8_STAGE(PG8_SB(0, 0), b2, voffB); PG8_STAGE(PG8_SB(0, 1), b2 + hstep, voffB); PG8_STAGE(PG8_SA(0, 0), a2, PG8_OS(0));
;             PG8_WAIT_V(8); PG8_WAIT_L(0); PG8_BAR; PG8_MMA(1, 0, At, B0); PG8_MMA(1, 1, At, B1); PG8_BAR; PG8_SCHED;
.LBB0_615:
	s_add_u32 s22, s20, 0xfff80080
	s_addc_u32 s23, s21, -1
	s_add_i32 s58, 0, 0x10000
	s_cmp_eq_u32 s57, 28
	s_cselect_b32 s25, s9, s23
	s_cselect_b32 s24, s17, s22
	s_cselect_b32 s23, s7, s56
	s_cselect_b32 s22, s19, s55
	s_add_i32 s60, 0, 0x14000
	v_add_u32_e32 v142, s58, v184
	v_add_u32_e32 v182, s60, v184
	ds_read_b128 v[122:125], v142
	ds_read_b128 v[126:129], v142 offset:1024
	ds_read_b128 v[134:137], v142 offset:2048
	ds_read_b128 v[142:145], v142 offset:3072
	ds_read_b128 v[174:177], v182
	ds_read_b128 v[178:181], v182 offset:1024
	ds_read_b128 v[188:191], v182 offset:2048
	ds_read_b128 v[192:195], v182 offset:3072
	v_lshl_add_u64 v[182:183], s[20:21], 0, v[170:171]
	s_add_i32 m0, s39, 0xc000
	ds_read_b128 v[196:199], v186
	ds_read_b128 v[200:203], v186 offset:1024
	ds_read_b128 v[204:207], v186 offset:2048
	ds_read_b128 v[208:211], v186 offset:3072
	ds_read_b128 v[212:215], v186 offset:4096
	ds_read_b128 v[216:219], v186 offset:5120
	ds_read_b128 v[220:223], v186 offset:6144
	ds_read_b128 v[224:227], v186 offset:7168
	global_load_lds_dwordx4 v[182:183], off
	v_lshl_add_u64 v[182:183], s[20:21], 0, v[172:173]
	s_add_i32 m0, s39, 0xe000
	s_nop 0
	global_load_lds_dwordx4 v[182:183], off
	s_waitcnt vmcnt(8)
	s_waitcnt lgkmcnt(0)
	v_mfma_f32_16x16x32_bf16 v[138:141], v[122:125], v[196:199], v[138:141]
	v_mfma_f32_16x16x32_bf16 v[130:133], v[134:137], v[196:199], v[130:133]
	v_mfma_f32_16x16x32_bf16 v[118:121], v[122:125], v[204:207], v[118:121]
	s_barrier
	s_setprio 1
	s_waitcnt lgkmcnt(0)
	v_mfma_f32_16x16x32_bf16 v[106:109], v[134:137], v[204:207], v[106:109]
	v_mfma_f32_16x16x32_bf16 v[102:105], v[122:125], v[212:215], v[102:105]
	v_mfma_f32_16x16x32_bf16 v[90:93], v[134:137], v[212:215], v[90:93]
	v_mfma_f32_16x16x32_bf16 v[86:89], v[122:125], v[220:223], v[86:89]
	v_mfma_f32_16x16x32_bf16 v[74:77], v[134:137], v[220:223], v[74:77]
	v_mfma_f32_16x16x32_bf16 v[138:141], v[126:129], v[200:203], v[138:141]
	v_mfma_f32_16x16x32_bf16 v[130:133], v[142:145], v[200:203], v[130:133]
	v_mfma_f32_16x16x32_bf16 v[118:121], v[126:129], v[208:211], v[118:121]
	v_mfma_f32_16x16x32_bf16 v[106:109], v[142:145], v[208:211], v[106:109]
	v_mfma_f32_16x16x32_bf16 v[102:105], v[126:129], v[216:219], v[102:105]
	v_mfma_f32_16x16x32_bf16 v[90:93], v[142:145], v[216:219], v[90:93]
	v_mfma_f32_16x16x32_bf16 v[86:89], v[126:129], v[224:227], v[86:89]
	v_mfma_f32_16x16x32_bf16 v[74:77], v[142:145], v[224:227], v[74:77]
	s_setprio 0
	s_setprio 1
	v_mfma_f32_16x16x32_bf16 v[114:117], v[174:177], v[196:199], v[114:117]
	v_mfma_f32_16x16x32_bf16 v[110:113], v[188:191], v[196:199], v[110:113]
	v_mfma_f32_16x16x32_bf16 v[98:101], v[174:177], v[204:207], v[98:101]
	v_mfma_f32_16x16x32_bf16 v[94:97], v[188:191], v[204:207], v[94:97]
	v_mfma_f32_16x16x32_bf16 v[82:85], v[174:177], v[212:215], v[82:85]
	v_mfma_f32_16x16x32_bf16 v[78:81], v[188:191], v[212:215], v[78:81]
	v_mfma_f32_16x16x32_bf16 v[70:73], v[174:177], v[220:223], v[70:73]
	v_mfma_f32_16x16x32_bf16 v[66:69], v[188:191], v[220:223], v[66:69]
	v_mfma_f32_16x16x32_bf16 v[114:117], v[178:181], v[200:203], v[114:117]
	v_mfma_f32_16x16x32_bf16 v[110:113], v[192:195], v[200:203], v[110:113]
	v_mfma_f32_16x16x32_bf16 v[98:101], v[178:181], v[208:211], v[98:101]
	v_mfma_f32_16x16x32_bf16 v[94:97], v[192:195], v[208:211], v[94:97]
	v_mfma_f32_16x16x32_bf16 v[82:85], v[178:181], v[216:219], v[82:85]
	v_mfma_f32_16x16x32_bf16 v[78:81], v[192:195], v[216:219], v[78:81]
	v_mfma_f32_16x16x32_bf16 v[70:73], v[178:181], v[224:227], v[70:73]
	v_mfma_f32_16x16x32_bf16 v[66:69], v[192:195], v[224:227], v[66:69]
	s_setprio 0
	s_barrier
	s_add_i32 s58, s58, s38
	v_lshl_add_u64 v[182:183], s[22:23], 0, v[0:1]
	s_mov_b32 m0, s58
	ds_read_b128 v[196:199], v186 offset:16384
	ds_read_b128 v[200:203], v186 offset:17408
	ds_read_b128 v[204:207], v186 offset:18432
	ds_read_b128 v[208:211], v186 offset:19456
	ds_read_b128 v[212:215], v186 offset:20480
	ds_read_b128 v[216:219], v186 offset:21504
	ds_read_b128 v[220:223], v186 offset:22528
	ds_read_b128 v[224:227], v186 offset:23552
	global_load_lds_dwordx4 v[182:183], off
	s_add_i32 m0, s58, 0x2000
	s_add_u32 s58, s22, 0x80000
	v_lshl_add_u64 v[228:229], s[22:23], 0, v[148:149]
	s_addc_u32 s59, s23, 0
	s_add_i32 s60, s60, s38
	global_load_lds_dwordx4 v[228:229], off
	v_lshl_add_u64 v[230:231], s[58:59], 0, v[0:1]
	s_mov_b32 m0, s60
	v_lshl_add_u64 v[232:233], s[24:25], 0, v[150:151]
	global_load_lds_dwordx4 v[230:231], off
	s_waitcnt vmcnt(5)
	s_waitcnt lgkmcnt(0)
	v_mfma_f32_16x16x32_bf16 v[62:65], v[122:125], v[196:199], v[62:65]
	v_mfma_f32_16x16x32_bf16 v[58:61], v[134:137], v[196:199], v[58:61]
	v_mfma_f32_16x16x32_bf16 v[54:57], v[122:125], v[204:207], v[54:57]
	s_barrier
; #define PG8_STAGE(bufoff, gbase, voff) do { _Pragma("unroll") for (int _i = 0; _i < 2; ++_i) \
;         __builtin_amdgcn_global_load_lds((const unsigned*)((const char*)(gbase) + (voff)[_i]), (PG8_LAS unsigned*)(lds + (bufoff) + ldsw + _i * 8192), 16, 0, 0); } while (0)
; #define PG8_LDA(dst, b, h) do { _Pragma("unroll") for (int m = 0; m < 4; ++m) _Pragma("unroll") for (int k = 0; k < 2; ++k) dst[m][k] = *(const PG8_LAS bf16x8*)(lds + PG8_SA(b, h) + aoff + m * 2048 + k * 1024); } while (0)
; #define PG8_LDB(dst, b, h) do { _Pragma("unroll") for (int n = 0; n < 2; ++n) _Pragma("unroll") for (int k = 0; k < 2; ++k) dst[n][k] = *(const PG8_LAS bf16x8*)(lds + PG8_SB(b, h) + boff + n * 2048 + k * 1024); } while (0)
; #define PG8_MMA(ai, bj, At, Bt) do { __builtin_amdgcn_s_setprio(1); _Pragma("unroll") for (int m = 0; m < 4; ++m) _Pragma("unroll") for (int n = 0; n < 2; ++n) _Pragma("unroll") for (int k = 0; k < 2; ++k) \
;         acc[ai][bj][m][n] = __builtin_amdgcn_mfma_f32_16x16x32_bf16(Bt[n][k], At[m][k], acc[ai][bj][m][n], 0, 0, 0); __builtin_amdgcn_s_setprio(0); } while (0)
; #define PG8_WAIT_V(n) asm volatile("s_waitcnt vmcnt(" #n ")" ::: "memory")
; #define PG8_WAIT_L(n) asm volatile("s_waitcnt lgkmcnt(" #n ")" ::: "memory")
; #define PG8_BAR __builtin_amdgcn_s_barrier()
; #define PG8_SCHED __builtin_amdgcn_sched_barrier(0)
; template <class Epi, class Sched, bool ALIGN_EPI = false, bool SP2 = false, bool GATHER = false>
; __device__ __forceinline__ void gemm_phase(PG8_LAS unsigned char* lds, const Gemm g, const Sched& S, const Epi& E, int tid_in, const int* rowsrc = nullptr, PG8_LAS int* idx_lds = nullptr) {
;     ...
;             PG8_WAIT_V(8); PG8_WAIT_L(0); PG8_BAR; PG8_MMA(1, 0, At, B0); PG8_MMA(1, 1, At, B1); PG8_BAR; PG8_SCHED;
;             PG8_LDB(B0, 1, 0); PG8_LDB(B1, 1, 1); PG8_SCHED; PG8_LDA(At, 1, 0); PG8_STAGE(PG8_SA(0, 1), a2 + hstepA, PG8_OS(1));
;             PG8_WAIT_V(8); PG8_WAIT_L(0); PG8_BAR; PG8_MMA(0, 0, At, B0); PG8_MMA(0, 1, At, B1); PG8_BAR; PG8_SCHED;
	s_setprio 1
	s_waitcnt lgkmcnt(0)
	v_mfma_f32_16x16x32_bf16 v[42:45], v[134:137], v[204:207], v[42:45]
	v_mfma_f32_16x16x32_bf16 v[38:41], v[122:125], v[212:215], v[38:41]
	v_mfma_f32_16x16x32_bf16 v[26:29], v[134:137], v[212:215], v[26:29]
	v_mfma_f32_16x16x32_bf16 v[22:25], v[122:125], v[220:223], v[22:25]
	v_mfma_f32_16x16x32_bf16 v[10:13], v[134:137], v[220:223], v[10:13]
	v_lshl_add_u64 v[230:231], s[58:59], 0, v[148:149]
	s_add_i32 m0, s60, 0x2000
	s_nop 0
	global_load_lds_dwordx4 v[230:231], off
	v_mfma_f32_16x16x32_bf16 v[62:65], v[126:129], v[200:203], v[62:65]
	v_mfma_f32_16x16x32_bf16 v[58:61], v[142:145], v[200:203], v[58:61]
	v_mfma_f32_16x16x32_bf16 v[54:57], v[126:129], v[208:211], v[54:57]
	v_mfma_f32_16x16x32_bf16 v[42:45], v[142:145], v[208:211], v[42:45]
	v_mfma_f32_16x16x32_bf16 v[38:41], v[126:129], v[216:219], v[38:41]
	v_mfma_f32_16x16x32_bf16 v[26:29], v[142:145], v[216:219], v[26:29]
	v_mfma_f32_16x16x32_bf16 v[22:25], v[126:129], v[224:227], v[22:25]
	v_mfma_f32_16x16x32_bf16 v[10:13], v[142:145], v[224:227], v[10:13]
	v_lshl_add_u64 v[230:231], s[24:25], 0, v[152:153]
	s_mov_b32 m0, s39
	s_nop 0
	global_load_lds_dwordx4 v[230:231], off
	s_setprio 0
	s_setprio 1
	v_mfma_f32_16x16x32_bf16 v[50:53], v[174:177], v[196:199], v[50:53]
	v_mfma_f32_16x16x32_bf16 v[46:49], v[188:191], v[196:199], v[46:49]
	v_mfma_f32_16x16x32_bf16 v[34:37], v[174:177], v[204:207], v[34:37]
	v_mfma_f32_16x16x32_bf16 v[30:33], v[188:191], v[204:207], v[30:33]
	v_mfma_f32_16x16x32_bf16 v[18:21], v[174:177], v[212:215], v[18:21]
	v_mfma_f32_16x16x32_bf16 v[14:17], v[188:191], v[212:215], v[14:17]
	v_mfma_f32_16x16x32_bf16 v[6:9], v[174:177], v[220:223], v[6:9]
	v_mfma_f32_16x16x32_bf16 v[2:5], v[188:191], v[220:223], v[2:5]
	s_mov_b32 m0, s41
	s_nop 0
	global_load_lds_dwordx4 v[232:233], off
	v_mfma_f32_16x16x32_bf16 v[50:53], v[178:181], v[200:203], v[50:53]
	v_mfma_f32_16x16x32_bf16 v[46:49], v[192:195], v[200:203], v[46:49]
	v_mfma_f32_16x16x32_bf16 v[34:37], v[178:181], v[208:211], v[34:37]
	v_mfma_f32_16x16x32_bf16 v[30:33], v[192:195], v[208:211], v[30:33]
	v_mfma_f32_16x16x32_bf16 v[18:21], v[178:181], v[216:219], v[18:21]
	v_mfma_f32_16x16x32_bf16 v[14:17], v[192:195], v[216:219], v[14:17]
	v_mfma_f32_16x16x32_bf16 v[6:9], v[178:181], v[224:227], v[6:9]
	v_mfma_f32_16x16x32_bf16 v[2:5], v[192:195], v[224:227], v[2:5]
	s_setprio 0
	s_barrier
	s_add_i32 s58, 0, 0x18000
	s_add_i32 s59, 0, 0x1c000
	v_add_u32_e32 v142, s58, v184
	v_add_u32_e32 v187, s59, v184
	ds_read_b128 v[122:125], v142
	ds_read_b128 v[126:129], v142 offset:1024
	ds_read_b128 v[134:137], v142 offset:2048
	ds_read_b128 v[142:145], v142 offset:3072
	ds_read_b128 v[174:177], v187
	ds_read_b128 v[178:181], v187 offset:1024
	ds_read_b128 v[188:191], v187 offset:2048
	ds_read_b128 v[192:195], v187 offset:3072
	s_add_u32 s24, s24, 0x80000
	s_addc_u32 s25, s25, 0
	s_mov_b32 m0, s43
	v_lshl_add_u64 v[234:235], s[24:25], 0, v[152:153]
	ds_read_b128 v[196:199], v186 offset:32768
	ds_read_b128 v[200:203], v186 offset:33792
	ds_read_b128 v[204:207], v186 offset:34816
	ds_read_b128 v[208:211], v186 offset:35840
	ds_read_b128 v[212:215], v186 offset:36864
	ds_read_b128 v[216:219], v186 offset:37888
	ds_read_b128 v[220:223], v186 offset:38912
	ds_read_b128 v[224:227], v186 offset:39936
	global_load_lds_dwordx4 v[234:235], off
	v_lshl_add_u64 v[234:235], s[24:25], 0, v[150:151]
	s_mov_b32 m0, s45
	s_nop 0
	global_load_lds_dwordx4 v[234:235], off
	s_waitcnt vmcnt(8)
	s_waitcnt lgkmcnt(0)
	v_mfma_f32_16x16x32_bf16 v[138:141], v[122:125], v[196:199], v[138:141]
	v_mfma_f32_16x16x32_bf16 v[130:133], v[134:137], v[196:199], v[130:133]
	v_mfma_f32_16x16x32_bf16 v[118:121], v[122:125], v[204:207], v[118:121]
	s_barrier
	s_setprio 1
	s_waitcnt lgkmcnt(0)
	v_mfma_f32_16x16x32_bf16 v[106:109], v[134:137], v[204:207], v[106:109]
	v_mfma_f32_16x16x32_bf16 v[102:105], v[122:125], v[212:215], v[102:105]
	v_mfma_f32_16x16x32_bf16 v[90:93], v[134:137], v[212:215], v[90:93]
	v_mfma_f32_16x16x32_bf16 v[86:89], v[122:125], v[220:223], v[86:89]
	v_mfma_f32_16x16x32_bf16 v[74:77], v[134:137], v[220:223], v[74:77]
	v_mfma_f32_16x16x32_bf16 v[138:141], v[126:129], v[200:203], v[138:141]
	v_mfma_f32_16x16x32_bf16 v[130:133], v[142:145], v[200:203], v[130:133]
	v_mfma_f32_16x16x32_bf16 v[118:121], v[126:129], v[208:211], v[118:121]
	v_mfma_f32_16x16x32_bf16 v[106:109], v[142:145], v[208:211], v[106:109]
	v_mfma_f32_16x16x32_bf16 v[102:105], v[126:129], v[216:219], v[102:105]
	v_mfma_f32_16x16x32_bf16 v[90:93], v[142:145], v[216:219], v[90:93]
	v_mfma_f32_16x16x32_bf16 v[86:89], v[126:129], v[224:227], v[86:89]
	v_mfma_f32_16x16x32_bf16 v[74:77], v[142:145], v[224:227], v[74:77]
	s_setprio 0
	s_setprio 1
	v_mfma_f32_16x16x32_bf16 v[114:117], v[174:177], v[196:199], v[114:117]
	v_mfma_f32_16x16x32_bf16 v[110:113], v[188:191], v[196:199], v[110:113]
	v_mfma_f32_16x16x32_bf16 v[98:101], v[174:177], v[204:207], v[98:101]
	v_mfma_f32_16x16x32_bf16 v[94:97], v[188:191], v[204:207], v[94:97]
	v_mfma_f32_16x16x32_bf16 v[82:85], v[174:177], v[212:215], v[82:85]
	v_mfma_f32_16x16x32_bf16 v[78:81], v[188:191], v[212:215], v[78:81]
	v_mfma_f32_16x16x32_bf16 v[70:73], v[174:177], v[220:223], v[70:73]
	v_mfma_f32_16x16x32_bf16 v[66:69], v[188:191], v[220:223], v[66:69]
	v_mfma_f32_16x16x32_bf16 v[114:117], v[178:181], v[200:203], v[114:117]
	v_mfma_f32_16x16x32_bf16 v[110:113], v[192:195], v[200:203], v[110:113]
	v_mfma_f32_16x16x32_bf16 v[98:101], v[178:181], v[208:211], v[98:101]
	v_mfma_f32_16x16x32_bf16 v[94:97], v[192:195], v[208:211], v[94:97]
	v_mfma_f32_16x16x32_bf16 v[82:85], v[178:181], v[216:219], v[82:85]
	v_mfma_f32_16x16x32_bf16 v[78:81], v[192:195], v[216:219], v[78:81]
	v_mfma_f32_16x16x32_bf16 v[70:73], v[178:181], v[224:227], v[70:73]
	v_mfma_f32_16x16x32_bf16 v[66:69], v[192:195], v[224:227], v[66:69]
	s_setprio 0
	s_barrier
; #define PG8_STAGE(bufoff, gbase, voff) do { _Pragma("unroll") for (int _i = 0; _i < 2; ++_i) \
;         __builtin_amdgcn_global_load_lds((const unsigned*)((const char*)(gbase) + (voff)[_i]), (PG8_LAS unsigned*)(lds + (bufoff) + ldsw + _i * 8192), 16, 0, 0); } while (0)
; #define PG8_LDA(dst, b, h) do { _Pragma("unroll") for (int m = 0; m < 4; ++m) _Pragma("unroll") for (int k = 0; k < 2; ++k) dst[m][k] = *(const PG8_LAS bf16x8*)(lds + PG8_SA(b, h) + aoff + m * 2048 + k * 1024); } while (0)
; #define PG8_MMA(ai, bj, At, Bt) do { __builtin_amdgcn_s_setprio(1); _Pragma("unroll") for (int m = 0; m < 4; ++m) _Pragma("unroll") for (int n = 0; n < 2; ++n) _Pragma("unroll") for (int k = 0; k < 2; ++k) \
;         acc[ai][bj][m][n] = __builtin_amdgcn_mfma_f32_16x16x32_bf16(Bt[n][k], At[m][k], acc[ai][bj][m][n], 0, 0, 0); __builtin_amdgcn_s_setprio(0); } while (0)
; #define PG8_WAIT_V(n) asm volatile("s_waitcnt vmcnt(" #n ")" ::: "memory")
; #define PG8_WAIT_L(n) asm volatile("s_waitcnt lgkmcnt(" #n ")" ::: "memory")
; #define PG8_BAR __builtin_amdgcn_s_barrier()
; #define PG8_SCHED __builtin_amdgcn_sched_barrier(0)
; template <class Epi, class Sched, bool ALIGN_EPI = false, bool SP2 = false, bool GATHER = false>
; __device__ __forceinline__ void gemm_phase(PG8_LAS unsigned char* lds, const Gemm g, const Sched& S, const Epi& E, int tid_in, const int* rowsrc = nullptr, PG8_LAS int* idx_lds = nullptr) {
;     ...
;             PG8_LDA(At, 1, 1); PG8_STAGE(PG8_SB(1, 0), b3, voffB); PG8_STAGE(PG8_SB(1, 1), b3 + hstep, voffB); PG8_STAGE(PG8_SA(1, 0), a3, PG8_OS(0));
;             PG8_WAIT_V(8); PG8_WAIT_L(0); PG8_BAR; PG8_MMA(1, 0, At, B0); PG8_MMA(1, 1, At, B1); PG8_BAR; PG8_SCHED;
;     ...
;         if constexpr (ALIGN_EPI) { if (wr == 0) PG8_BAR; }
	s_add_i32 s24, s58, s38
	v_lshl_add_u64 v[182:183], v[182:183], 0, s[10:11]
	s_mov_b32 m0, s24
	ds_read_b128 v[196:199], v186 offset:49152
	ds_read_b128 v[200:203], v186 offset:50176
	ds_read_b128 v[204:207], v186 offset:51200
	ds_read_b128 v[208:211], v186 offset:52224
	ds_read_b128 v[212:215], v186 offset:53248
	ds_read_b128 v[216:219], v186 offset:54272
	ds_read_b128 v[220:223], v186 offset:55296
	ds_read_b128 v[224:227], v186 offset:56320
	global_load_lds_dwordx4 v[182:183], off
	s_add_i32 m0, s24, 0x2000
	s_add_u32 s22, s22, 0x80080
	v_lshl_add_u64 v[182:183], v[228:229], 0, s[10:11]
	s_addc_u32 s23, s23, 0
	s_add_i32 s24, s59, s38
	global_load_lds_dwordx4 v[182:183], off
	v_lshl_add_u64 v[182:183], s[22:23], 0, v[0:1]
	s_mov_b32 m0, s24
	s_nop 0
	global_load_lds_dwordx4 v[182:183], off
	s_waitcnt vmcnt(5)
	s_waitcnt lgkmcnt(0)
	v_mfma_f32_16x16x32_bf16 v[62:65], v[122:125], v[196:199], v[62:65]
	v_mfma_f32_16x16x32_bf16 v[58:61], v[134:137], v[196:199], v[58:61]
	v_mfma_f32_16x16x32_bf16 v[54:57], v[122:125], v[204:207], v[54:57]
	s_barrier
	s_setprio 1
	s_waitcnt lgkmcnt(0)
	v_mfma_f32_16x16x32_bf16 v[42:45], v[134:137], v[204:207], v[42:45]
	v_mfma_f32_16x16x32_bf16 v[38:41], v[122:125], v[212:215], v[38:41]
	v_mfma_f32_16x16x32_bf16 v[26:29], v[134:137], v[212:215], v[26:29]
	v_mfma_f32_16x16x32_bf16 v[22:25], v[122:125], v[220:223], v[22:25]
	v_mfma_f32_16x16x32_bf16 v[10:13], v[134:137], v[220:223], v[10:13]
	v_lshl_add_u64 v[182:183], s[22:23], 0, v[148:149]
	s_add_i32 m0, s24, 0x2000
	s_nop 0
	global_load_lds_dwordx4 v[182:183], off
	v_mfma_f32_16x16x32_bf16 v[62:65], v[126:129], v[200:203], v[62:65]
	v_mfma_f32_16x16x32_bf16 v[58:61], v[142:145], v[200:203], v[58:61]
	v_mfma_f32_16x16x32_bf16 v[54:57], v[126:129], v[208:211], v[54:57]
	v_mfma_f32_16x16x32_bf16 v[42:45], v[142:145], v[208:211], v[42:45]
	v_mfma_f32_16x16x32_bf16 v[38:41], v[126:129], v[216:219], v[38:41]
	v_mfma_f32_16x16x32_bf16 v[26:29], v[142:145], v[216:219], v[26:29]
	v_mfma_f32_16x16x32_bf16 v[22:25], v[126:129], v[224:227], v[22:25]
	v_mfma_f32_16x16x32_bf16 v[10:13], v[142:145], v[224:227], v[10:13]
	v_lshl_add_u64 v[182:183], v[230:231], 0, s[10:11]
	s_mov_b32 m0, s52
	s_nop 0
	global_load_lds_dwordx4 v[182:183], off
	s_setprio 0
	s_setprio 1
	v_mfma_f32_16x16x32_bf16 v[50:53], v[174:177], v[196:199], v[50:53]
	v_mfma_f32_16x16x32_bf16 v[46:49], v[188:191], v[196:199], v[46:49]
	v_mfma_f32_16x16x32_bf16 v[34:37], v[174:177], v[204:207], v[34:37]
	v_mfma_f32_16x16x32_bf16 v[30:33], v[188:191], v[204:207], v[30:33]
	v_mfma_f32_16x16x32_bf16 v[18:21], v[174:177], v[212:215], v[18:21]
	v_mfma_f32_16x16x32_bf16 v[14:17], v[188:191], v[212:215], v[14:17]
	v_mfma_f32_16x16x32_bf16 v[6:9], v[174:177], v[220:223], v[6:9]
	v_mfma_f32_16x16x32_bf16 v[2:5], v[188:191], v[220:223], v[2:5]
	v_lshl_add_u64 v[182:183], v[232:233], 0, s[10:11]
	s_mov_b32 m0, s53
	s_nop 0
	global_load_lds_dwordx4 v[182:183], off
	v_mfma_f32_16x16x32_bf16 v[50:53], v[178:181], v[200:203], v[50:53]
	v_mfma_f32_16x16x32_bf16 v[46:49], v[192:195], v[200:203], v[46:49]
	v_mfma_f32_16x16x32_bf16 v[34:37], v[178:181], v[208:211], v[34:37]
	v_mfma_f32_16x16x32_bf16 v[30:33], v[192:195], v[208:211], v[30:33]
	v_mfma_f32_16x16x32_bf16 v[18:21], v[178:181], v[216:219], v[18:21]
	v_mfma_f32_16x16x32_bf16 v[14:17], v[192:195], v[216:219], v[14:17]
	v_mfma_f32_16x16x32_bf16 v[6:9], v[178:181], v[224:227], v[6:9]
	v_mfma_f32_16x16x32_bf16 v[2:5], v[192:195], v[224:227], v[2:5]
	s_setprio 0
	s_barrier
	s_add_i32 s57, s57, 2
	s_add_u32 s20, s20, 0x100
	s_addc_u32 s21, s21, 0
	s_add_u32 s55, s55, 0x100
	s_addc_u32 s56, s56, 0
	s_cmp_gt_u32 s57, 29
	s_cbranch_scc0 .LBB0_615
	s_and_b64 vcc, exec, s[4:5]
	s_cbranch_vccz .LBB0_618
	s_barrier

; #define PG8_STAGE(bufoff, gbase, voff) do { _Pragma("unroll") for (int _i = 0; _i < 2; ++_i) \
;         __builtin_amdgcn_global_load_lds((const unsigned*)((const char*)(gbase) + (voff)[_i]), (PG8_LAS unsigned*)(lds + (bufoff) + ldsw + _i * 8192), 16, 0, 0); } while (0)
; #define PG8_LDA(dst, b, h) do { _Pragma("unroll") for (int m = 0; m < 4; ++m) _Pragma("unroll") for (int k = 0; k < 2; ++k) dst[m][k] = *(const PG8_LAS bf16x8*)(lds + PG8_SA(b, h) + aoff + m * 2048 + k * 1024); } while (0)
; #define PG8_LDB(dst, b, h) do { _Pragma("unroll") for (int n = 0; n < 2; ++n) _Pragma("unroll") for (int k = 0; k < 2; ++k) dst[n][k] = *(const PG8_LAS bf16x8*)(lds + PG8_SB(b, h) + boff + n * 2048 + k * 1024); } while (0)
; #define PG8_WAIT_V(n) asm volatile("s_waitcnt vmcnt(" #n ")" ::: "memory")
; #define PG8_WAIT_L(n) asm volatile("s_waitcnt lgkmcnt(" #n ")" ::: "memory")
; #define PG8_BAR __builtin_amdgcn_s_barrier()
; template <class Epi, class Sched, bool ALIGN_EPI = false, bool SP2 = false, bool GATHER = false>
; __device__ __forceinline__ void gemm_phase(PG8_LAS unsigned char* lds, const Gemm g, const Sched& S, const Epi& E, int tid_in, const int* rowsrc = nullptr, PG8_LAS int* idx_lds = nullptr) {
;     ...
;         for (int t = 0; t < nt; t += 2) {
;             const bool last = (t == nt - 2);
;             if constexpr (GATHER) {
; #pragma unroll
;                 for (int h_ = 0; h_ < 2; ++h_) { gS[h_][0] = last ? gN[h_][0] : gA[h_][0]; gS[h_][1] = last ? gN[h_][1] : gA[h_][1]; } }
;             const char* a1 = cA + (size_t)(t + 1) * kstep;
;             const char* a2 = last ? nA : cA + (size_t)(t + 2) * kstep; const char* b2 = last ? nB : cB + (size_t)(t + 2) * kstep;
;             const char* a3 = a2 + kstep; const char* b3 = b2 + kstep;
;             if (last && has_next) S.a_ready(nxt);
;             if constexpr (SP2) {
;             PG8_LDB(B0, 0, 0); PG8_LDB(B1, 0, 1); PG8_SCHED; PG8_LDA(At, 0, 0); PG8_STAGE(PG8_SA(1, 1), a1 + hstepA, PG8_OA(1));
;             PG8_WAIT_V(8); PG8_WAIT_L(0); PG8_BAR; PG8_MMA(0, 0, At, B0); PG8_MMA(0, 1, At, B1); PG8_BAR; PG8_SCHED;
;             PG8_LDA(At, 0, 1); PG8_STAGE(PG8_SB(0, 0), b2, voffB); PG8_STAGE(PG8_SB(0, 1), b2 + hstep, voffB); PG8_STAGE(PG8_SA(0, 0), a2, PG8_OS(0));
;             PG8_WAIT_V(8); PG8_WAIT_L(0); PG8_BAR; PG8_MMA(1, 0, At, B0); PG8_MMA(1, 1, At, B1); PG8_BAR; PG8_SCHED;
.LBB0_692:
	s_add_u32 s22, s20, 0xfffc0080
	s_addc_u32 s23, s21, -1
	s_add_i32 s52, 0, 0x10000
	s_cmp_eq_u32 s51, 12
	s_cselect_b32 s25, s15, s23
	s_cselect_b32 s24, s47, s22
	s_cselect_b32 s23, s13, s50
	s_cselect_b32 s22, s48, s49
	s_add_i32 s54, 0, 0x14000
	v_add_u32_e32 v158, s52, v145
	v_add_u32_e32 v174, s54, v145
	ds_read_b128 v[140:143], v158
	ds_read_b128 v[150:153], v158 offset:1024
	ds_read_b128 v[154:157], v158 offset:2048
	ds_read_b128 v[158:161], v158 offset:3072
	ds_read_b128 v[162:165], v174
	ds_read_b128 v[166:169], v174 offset:1024
	ds_read_b128 v[170:173], v174 offset:2048
	ds_read_b128 v[174:177], v174 offset:3072
	v_lshl_add_u64 v[178:179], s[20:21], 0, v[136:137]
	s_add_i32 m0, s31, 0xc000
	ds_read_b128 v[184:187], v149
	ds_read_b128 v[188:191], v149 offset:1024
	ds_read_b128 v[192:195], v149 offset:2048
	ds_read_b128 v[196:199], v149 offset:3072
	ds_read_b128 v[200:203], v149 offset:4096
	ds_read_b128 v[204:207], v149 offset:5120
	ds_read_b128 v[208:211], v149 offset:6144
	ds_read_b128 v[212:215], v149 offset:7168
	global_load_lds_dwordx4 v[178:179], off
	v_lshl_add_u64 v[178:179], s[20:21], 0, v[138:139]
	s_add_i32 m0, s31, 0xe000
	s_nop 0
	global_load_lds_dwordx4 v[178:179], off
	s_waitcnt vmcnt(8)
	s_waitcnt lgkmcnt(0)
	v_mfma_f32_16x16x32_bf16 v[126:129], v[140:143], v[184:187], v[126:129]
	v_mfma_f32_16x16x32_bf16 v[122:125], v[154:157], v[184:187], v[122:125]
	v_mfma_f32_16x16x32_bf16 v[118:121], v[140:143], v[192:195], v[118:121]
	s_barrier
	s_setprio 1
	s_waitcnt lgkmcnt(0)
	v_mfma_f32_16x16x32_bf16 v[110:113], v[154:157], v[192:195], v[110:113]
	v_mfma_f32_16x16x32_bf16 v[102:105], v[140:143], v[200:203], v[102:105]
	v_mfma_f32_16x16x32_bf16 v[94:97], v[154:157], v[200:203], v[94:97]
	v_mfma_f32_16x16x32_bf16 v[86:89], v[140:143], v[208:211], v[86:89]
	v_mfma_f32_16x16x32_bf16 v[78:81], v[154:157], v[208:211], v[78:81]
	v_mfma_f32_16x16x32_bf16 v[126:129], v[150:153], v[188:191], v[126:129]
	v_mfma_f32_16x16x32_bf16 v[122:125], v[158:161], v[188:191], v[122:125]
	v_mfma_f32_16x16x32_bf16 v[118:121], v[150:153], v[196:199], v[118:121]
	v_mfma_f32_16x16x32_bf16 v[110:113], v[158:161], v[196:199], v[110:113]
	v_mfma_f32_16x16x32_bf16 v[102:105], v[150:153], v[204:207], v[102:105]
	v_mfma_f32_16x16x32_bf16 v[94:97], v[158:161], v[204:207], v[94:97]
	v_mfma_f32_16x16x32_bf16 v[86:89], v[150:153], v[212:215], v[86:89]
	v_mfma_f32_16x16x32_bf16 v[78:81], v[158:161], v[212:215], v[78:81]
	s_setprio 0
	s_setprio 1
	v_mfma_f32_16x16x32_bf16 v[114:117], v[162:165], v[184:187], v[114:117]
	v_mfma_f32_16x16x32_bf16 v[106:109], v[170:173], v[184:187], v[106:109]
	v_mfma_f32_16x16x32_bf16 v[98:101], v[162:165], v[192:195], v[98:101]
	v_mfma_f32_16x16x32_bf16 v[90:93], v[170:173], v[192:195], v[90:93]
	v_mfma_f32_16x16x32_bf16 v[82:85], v[162:165], v[200:203], v[82:85]
	v_mfma_f32_16x16x32_bf16 v[74:77], v[170:173], v[200:203], v[74:77]
	v_mfma_f32_16x16x32_bf16 v[70:73], v[162:165], v[208:211], v[70:73]
	v_mfma_f32_16x16x32_bf16 v[66:69], v[170:173], v[208:211], v[66:69]
	v_mfma_f32_16x16x32_bf16 v[114:117], v[166:169], v[188:191], v[114:117]
	v_mfma_f32_16x16x32_bf16 v[106:109], v[174:177], v[188:191], v[106:109]
	v_mfma_f32_16x16x32_bf16 v[98:101], v[166:169], v[196:199], v[98:101]
	v_mfma_f32_16x16x32_bf16 v[90:93], v[174:177], v[196:199], v[90:93]
	v_mfma_f32_16x16x32_bf16 v[82:85], v[166:169], v[204:207], v[82:85]
	v_mfma_f32_16x16x32_bf16 v[74:77], v[174:177], v[204:207], v[74:77]
	v_mfma_f32_16x16x32_bf16 v[70:73], v[166:169], v[212:215], v[70:73]
	v_mfma_f32_16x16x32_bf16 v[66:69], v[174:177], v[212:215], v[66:69]
	s_setprio 0
	s_barrier
	s_add_i32 s52, s52, s30
	v_lshl_add_u64 v[178:179], s[22:23], 0, v[0:1]
	s_mov_b32 m0, s52
	ds_read_b128 v[184:187], v149 offset:16384
	ds_read_b128 v[188:191], v149 offset:17408
	ds_read_b128 v[192:195], v149 offset:18432
	ds_read_b128 v[196:199], v149 offset:19456
	ds_read_b128 v[200:203], v149 offset:20480
	ds_read_b128 v[204:207], v149 offset:21504
	ds_read_b128 v[208:211], v149 offset:22528
	ds_read_b128 v[212:215], v149 offset:23552
	global_load_lds_dwordx4 v[178:179], off
	s_add_i32 m0, s52, 0x2000
	s_add_u32 s52, s22, 0x40000
	v_lshl_add_u64 v[180:181], s[22:23], 0, v[130:131]
	s_addc_u32 s53, s23, 0
	s_add_i32 s54, s54, s30
	global_load_lds_dwordx4 v[180:181], off
	v_lshl_add_u64 v[182:183], s[52:53], 0, v[0:1]
	s_mov_b32 m0, s54
	v_lshl_add_u64 v[216:217], s[24:25], 0, v[132:133]
	global_load_lds_dwordx4 v[182:183], off
	s_waitcnt vmcnt(5)
	s_waitcnt lgkmcnt(0)
	v_mfma_f32_16x16x32_bf16 v[62:65], v[140:143], v[184:187], v[62:65]
	v_mfma_f32_16x16x32_bf16 v[58:61], v[154:157], v[184:187], v[58:61]
	v_mfma_f32_16x16x32_bf16 v[54:57], v[140:143], v[192:195], v[54:57]
	s_barrier
; #define PG8_STAGE(bufoff, gbase, voff) do { _Pragma("unroll") for (int _i = 0; _i < 2; ++_i) \
;         __builtin_amdgcn_global_load_lds((const unsigned*)((const char*)(gbase) + (voff)[_i]), (PG8_LAS unsigned*)(lds + (bufoff) + ldsw + _i * 8192), 16, 0, 0); } while (0)
; #define PG8_LDA(dst, b, h) do { _Pragma("unroll") for (int m = 0; m < 4; ++m) _Pragma("unroll") for (int k = 0; k < 2; ++k) dst[m][k] = *(const PG8_LAS bf16x8*)(lds + PG8_SA(b, h) + aoff + m * 2048 + k * 1024); } while (0)
; #define PG8_LDB(dst, b, h) do { _Pragma("unroll") for (int n = 0; n < 2; ++n) _Pragma("unroll") for (int k = 0; k < 2; ++k) dst[n][k] = *(const PG8_LAS bf16x8*)(lds + PG8_SB(b, h) + boff + n * 2048 + k * 1024); } while (0)
; #define PG8_MMA(ai, bj, At, Bt) do { __builtin_amdgcn_s_setprio(1); _Pragma("unroll") for (int m = 0; m < 4; ++m) _Pragma("unroll") for (int n = 0; n < 2; ++n) _Pragma("unroll") for (int k = 0; k < 2; ++k) \
;         acc[ai][bj][m][n] = __builtin_amdgcn_mfma_f32_16x16x32_bf16(Bt[n][k], At[m][k], acc[ai][bj][m][n], 0, 0, 0); __builtin_amdgcn_s_setprio(0); } while (0)
; #define PG8_WAIT_V(n) asm volatile("s_waitcnt vmcnt(" #n ")" ::: "memory")
; #define PG8_WAIT_L(n) asm volatile("s_waitcnt lgkmcnt(" #n ")" ::: "memory")
; #define PG8_BAR __builtin_amdgcn_s_barrier()
; #define PG8_SCHED __builtin_amdgcn_sched_barrier(0)
; template <class Epi, class Sched, bool ALIGN_EPI = false, bool SP2 = false, bool GATHER = false>
; __device__ __forceinline__ void gemm_phase(PG8_LAS unsigned char* lds, const Gemm g, const Sched& S, const Epi& E, int tid_in, const int* rowsrc = nullptr, PG8_LAS int* idx_lds = nullptr) {
;     ...
;             PG8_WAIT_V(8); PG8_WAIT_L(0); PG8_BAR; PG8_MMA(1, 0, At, B0); PG8_MMA(1, 1, At, B1); PG8_BAR; PG8_SCHED;
;             PG8_LDB(B0, 1, 0); PG8_LDB(B1, 1, 1); PG8_SCHED; PG8_LDA(At, 1, 0); PG8_STAGE(PG8_SA(0, 1), a2 + hstepA, PG8_OS(1));
;             PG8_WAIT_V(8); PG8_WAIT_L(0); PG8_BAR; PG8_MMA(0, 0, At, B0); PG8_MMA(0, 1, At, B1); PG8_BAR; PG8_SCHED;
	s_setprio 1
	s_waitcnt lgkmcnt(0)
	v_mfma_f32_16x16x32_bf16 v[46:49], v[154:157], v[192:195], v[46:49]
	v_mfma_f32_16x16x32_bf16 v[38:41], v[140:143], v[200:203], v[38:41]
	v_mfma_f32_16x16x32_bf16 v[30:33], v[154:157], v[200:203], v[30:33]
	v_mfma_f32_16x16x32_bf16 v[22:25], v[140:143], v[208:211], v[22:25]
	v_mfma_f32_16x16x32_bf16 v[14:17], v[154:157], v[208:211], v[14:17]
	v_lshl_add_u64 v[182:183], s[52:53], 0, v[130:131]
	s_add_i32 m0, s54, 0x2000
	s_nop 0
	global_load_lds_dwordx4 v[182:183], off
	v_mfma_f32_16x16x32_bf16 v[62:65], v[150:153], v[188:191], v[62:65]
	v_mfma_f32_16x16x32_bf16 v[58:61], v[158:161], v[188:191], v[58:61]
	v_mfma_f32_16x16x32_bf16 v[54:57], v[150:153], v[196:199], v[54:57]
	v_mfma_f32_16x16x32_bf16 v[46:49], v[158:161], v[196:199], v[46:49]
	v_mfma_f32_16x16x32_bf16 v[38:41], v[150:153], v[204:207], v[38:41]
	v_mfma_f32_16x16x32_bf16 v[30:33], v[158:161], v[204:207], v[30:33]
	v_mfma_f32_16x16x32_bf16 v[22:25], v[150:153], v[212:215], v[22:25]
	v_mfma_f32_16x16x32_bf16 v[14:17], v[158:161], v[212:215], v[14:17]
	v_lshl_add_u64 v[182:183], s[24:25], 0, v[134:135]
	s_mov_b32 m0, s31
	s_nop 0
	global_load_lds_dwordx4 v[182:183], off
	s_setprio 0
	s_setprio 1
	v_mfma_f32_16x16x32_bf16 v[50:53], v[162:165], v[184:187], v[50:53]
	v_mfma_f32_16x16x32_bf16 v[42:45], v[170:173], v[184:187], v[42:45]
	v_mfma_f32_16x16x32_bf16 v[34:37], v[162:165], v[192:195], v[34:37]
	v_mfma_f32_16x16x32_bf16 v[26:29], v[170:173], v[192:195], v[26:29]
	v_mfma_f32_16x16x32_bf16 v[18:21], v[162:165], v[200:203], v[18:21]
	v_mfma_f32_16x16x32_bf16 v[10:13], v[170:173], v[200:203], v[10:13]
	v_mfma_f32_16x16x32_bf16 v[6:9], v[162:165], v[208:211], v[6:9]
	v_mfma_f32_16x16x32_bf16 v[2:5], v[170:173], v[208:211], v[2:5]
	s_mov_b32 m0, s34
	s_nop 0
	global_load_lds_dwordx4 v[216:217], off
	v_mfma_f32_16x16x32_bf16 v[50:53], v[166:169], v[188:191], v[50:53]
	v_mfma_f32_16x16x32_bf16 v[42:45], v[174:177], v[188:191], v[42:45]
	v_mfma_f32_16x16x32_bf16 v[34:37], v[166:169], v[196:199], v[34:37]
	v_mfma_f32_16x16x32_bf16 v[26:29], v[174:177], v[196:199], v[26:29]
	v_mfma_f32_16x16x32_bf16 v[18:21], v[166:169], v[204:207], v[18:21]
	v_mfma_f32_16x16x32_bf16 v[10:13], v[174:177], v[204:207], v[10:13]
	v_mfma_f32_16x16x32_bf16 v[6:9], v[166:169], v[212:215], v[6:9]
	v_mfma_f32_16x16x32_bf16 v[2:5], v[174:177], v[212:215], v[2:5]
	s_setprio 0
	s_barrier
	s_add_i32 s52, 0, 0x18000
	s_add_i32 s53, 0, 0x1c000
	v_add_u32_e32 v158, s52, v145
	v_add_u32_e32 v174, s53, v145
	ds_read_b128 v[140:143], v158
	ds_read_b128 v[150:153], v158 offset:1024
	ds_read_b128 v[154:157], v158 offset:2048
	ds_read_b128 v[158:161], v158 offset:3072
	ds_read_b128 v[162:165], v174
	ds_read_b128 v[166:169], v174 offset:1024
	ds_read_b128 v[170:173], v174 offset:2048
	ds_read_b128 v[174:177], v174 offset:3072
	s_add_u32 s24, s24, 0x40000
	s_addc_u32 s25, s25, 0
	s_mov_b32 m0, s35
	v_lshl_add_u64 v[218:219], s[24:25], 0, v[134:135]
	ds_read_b128 v[184:187], v149 offset:32768
	ds_read_b128 v[188:191], v149 offset:33792
	ds_read_b128 v[192:195], v149 offset:34816
	ds_read_b128 v[196:199], v149 offset:35840
	ds_read_b128 v[200:203], v149 offset:36864
	ds_read_b128 v[204:207], v149 offset:37888
	ds_read_b128 v[208:211], v149 offset:38912
	ds_read_b128 v[212:215], v149 offset:39936
	global_load_lds_dwordx4 v[218:219], off
	v_lshl_add_u64 v[218:219], s[24:25], 0, v[132:133]
	s_mov_b32 m0, s36
	s_nop 0
	global_load_lds_dwordx4 v[218:219], off
	s_waitcnt vmcnt(8)
	s_waitcnt lgkmcnt(0)
	v_mfma_f32_16x16x32_bf16 v[126:129], v[140:143], v[184:187], v[126:129]
	v_mfma_f32_16x16x32_bf16 v[122:125], v[154:157], v[184:187], v[122:125]
	v_mfma_f32_16x16x32_bf16 v[118:121], v[140:143], v[192:195], v[118:121]
	s_barrier
	s_setprio 1
	s_waitcnt lgkmcnt(0)
	v_mfma_f32_16x16x32_bf16 v[110:113], v[154:157], v[192:195], v[110:113]
	v_mfma_f32_16x16x32_bf16 v[102:105], v[140:143], v[200:203], v[102:105]
	v_mfma_f32_16x16x32_bf16 v[94:97], v[154:157], v[200:203], v[94:97]
	v_mfma_f32_16x16x32_bf16 v[86:89], v[140:143], v[208:211], v[86:89]
	v_mfma_f32_16x16x32_bf16 v[78:81], v[154:157], v[208:211], v[78:81]
	v_mfma_f32_16x16x32_bf16 v[126:129], v[150:153], v[188:191], v[126:129]
	v_mfma_f32_16x16x32_bf16 v[122:125], v[158:161], v[188:191], v[122:125]
	v_mfma_f32_16x16x32_bf16 v[118:121], v[150:153], v[196:199], v[118:121]
	v_mfma_f32_16x16x32_bf16 v[110:113], v[158:161], v[196:199], v[110:113]
	v_mfma_f32_16x16x32_bf16 v[102:105], v[150:153], v[204:207], v[102:105]
	v_mfma_f32_16x16x32_bf16 v[94:97], v[158:161], v[204:207], v[94:97]
	v_mfma_f32_16x16x32_bf16 v[86:89], v[150:153], v[212:215], v[86:89]
	v_mfma_f32_16x16x32_bf16 v[78:81], v[158:161], v[212:215], v[78:81]
	s_setprio 0
	s_setprio 1
	v_mfma_f32_16x16x32_bf16 v[114:117], v[162:165], v[184:187], v[114:117]
	v_mfma_f32_16x16x32_bf16 v[106:109], v[170:173], v[184:187], v[106:109]
	v_mfma_f32_16x16x32_bf16 v[98:101], v[162:165], v[192:195], v[98:101]
	v_mfma_f32_16x16x32_bf16 v[90:93], v[170:173], v[192:195], v[90:93]
	v_mfma_f32_16x16x32_bf16 v[82:85], v[162:165], v[200:203], v[82:85]
	v_mfma_f32_16x16x32_bf16 v[74:77], v[170:173], v[200:203], v[74:77]
	v_mfma_f32_16x16x32_bf16 v[70:73], v[162:165], v[208:211], v[70:73]
	v_mfma_f32_16x16x32_bf16 v[66:69], v[170:173], v[208:211], v[66:69]
	v_mfma_f32_16x16x32_bf16 v[114:117], v[166:169], v[188:191], v[114:117]
	v_mfma_f32_16x16x32_bf16 v[106:109], v[174:177], v[188:191], v[106:109]
	v_mfma_f32_16x16x32_bf16 v[98:101], v[166:169], v[196:199], v[98:101]
	v_mfma_f32_16x16x32_bf16 v[90:93], v[174:177], v[196:199], v[90:93]
	v_mfma_f32_16x16x32_bf16 v[82:85], v[166:169], v[204:207], v[82:85]
	v_mfma_f32_16x16x32_bf16 v[74:77], v[174:177], v[204:207], v[74:77]
	v_mfma_f32_16x16x32_bf16 v[70:73], v[166:169], v[212:215], v[70:73]
	v_mfma_f32_16x16x32_bf16 v[66:69], v[174:177], v[212:215], v[66:69]
	s_setprio 0
	s_barrier
; #define PG8_STAGE(bufoff, gbase, voff) do { _Pragma("unroll") for (int _i = 0; _i < 2; ++_i) \
;         __builtin_amdgcn_global_load_lds((const unsigned*)((const char*)(gbase) + (voff)[_i]), (PG8_LAS unsigned*)(lds + (bufoff) + ldsw + _i * 8192), 16, 0, 0); } while (0)
; #define PG8_LDA(dst, b, h) do { _Pragma("unroll") for (int m = 0; m < 4; ++m) _Pragma("unroll") for (int k = 0; k < 2; ++k) dst[m][k] = *(const PG8_LAS bf16x8*)(lds + PG8_SA(b, h) + aoff + m * 2048 + k * 1024); } while (0)
; #define PG8_MMA(ai, bj, At, Bt) do { __builtin_amdgcn_s_setprio(1); _Pragma("unroll") for (int m = 0; m < 4; ++m) _Pragma("unroll") for (int n = 0; n < 2; ++n) _Pragma("unroll") for (int k = 0; k < 2; ++k) \
;         acc[ai][bj][m][n] = __builtin_amdgcn_mfma_f32_16x16x32_bf16(Bt[n][k], At[m][k], acc[ai][bj][m][n], 0, 0, 0); __builtin_amdgcn_s_setprio(0); } while (0)
; #define PG8_WAIT_V(n) asm volatile("s_waitcnt vmcnt(" #n ")" ::: "memory")
; #define PG8_WAIT_L(n) asm volatile("s_waitcnt lgkmcnt(" #n ")" ::: "memory")
; #define PG8_BAR __builtin_amdgcn_s_barrier()
; #define PG8_SCHED __builtin_amdgcn_sched_barrier(0)
; template <class Epi, class Sched, bool ALIGN_EPI = false, bool SP2 = false, bool GATHER = false>
; __device__ __forceinline__ void gemm_phase(PG8_LAS unsigned char* lds, const Gemm g, const Sched& S, const Epi& E, int tid_in, const int* rowsrc = nullptr, PG8_LAS int* idx_lds = nullptr) {
;     ...
;             PG8_LDA(At, 1, 1); PG8_STAGE(PG8_SB(1, 0), b3, voffB); PG8_STAGE(PG8_SB(1, 1), b3 + hstep, voffB); PG8_STAGE(PG8_SA(1, 0), a3, PG8_OS(0));
;             PG8_WAIT_V(8); PG8_WAIT_L(0); PG8_BAR; PG8_MMA(1, 0, At, B0); PG8_MMA(1, 1, At, B1); PG8_BAR; PG8_SCHED;
;     ...
;         if constexpr (ALIGN_EPI) { if (wr == 0) PG8_BAR; }
	s_add_i32 s24, s52, s30
	v_lshl_add_u64 v[178:179], v[178:179], 0, s[10:11]
	s_mov_b32 m0, s24
	ds_read_b128 v[184:187], v149 offset:49152
	ds_read_b128 v[188:191], v149 offset:50176
	ds_read_b128 v[192:195], v149 offset:51200
	ds_read_b128 v[196:199], v149 offset:52224
	ds_read_b128 v[200:203], v149 offset:53248
	ds_read_b128 v[204:207], v149 offset:54272
	ds_read_b128 v[208:211], v149 offset:55296
	ds_read_b128 v[212:215], v149 offset:56320
	global_load_lds_dwordx4 v[178:179], off
	s_add_i32 m0, s24, 0x2000
	s_add_u32 s22, s22, 0x40080
	v_lshl_add_u64 v[178:179], v[180:181], 0, s[10:11]
	s_addc_u32 s23, s23, 0
	s_add_i32 s24, s53, s30
	global_load_lds_dwordx4 v[178:179], off
	v_lshl_add_u64 v[178:179], s[22:23], 0, v[0:1]
	s_mov_b32 m0, s24
	s_nop 0
	global_load_lds_dwordx4 v[178:179], off
	s_waitcnt vmcnt(5)
	s_waitcnt lgkmcnt(0)
	v_mfma_f32_16x16x32_bf16 v[62:65], v[140:143], v[184:187], v[62:65]
	v_mfma_f32_16x16x32_bf16 v[58:61], v[154:157], v[184:187], v[58:61]
	v_mfma_f32_16x16x32_bf16 v[54:57], v[140:143], v[192:195], v[54:57]
	s_barrier
	s_setprio 1
	s_waitcnt lgkmcnt(0)
	v_mfma_f32_16x16x32_bf16 v[46:49], v[154:157], v[192:195], v[46:49]
	v_mfma_f32_16x16x32_bf16 v[38:41], v[140:143], v[200:203], v[38:41]
	v_mfma_f32_16x16x32_bf16 v[30:33], v[154:157], v[200:203], v[30:33]
	v_mfma_f32_16x16x32_bf16 v[22:25], v[140:143], v[208:211], v[22:25]
	v_mfma_f32_16x16x32_bf16 v[14:17], v[154:157], v[208:211], v[14:17]
	v_lshl_add_u64 v[178:179], s[22:23], 0, v[130:131]
	s_add_i32 m0, s24, 0x2000
	s_nop 0
	global_load_lds_dwordx4 v[178:179], off
	v_mfma_f32_16x16x32_bf16 v[62:65], v[150:153], v[188:191], v[62:65]
	v_mfma_f32_16x16x32_bf16 v[58:61], v[158:161], v[188:191], v[58:61]
	v_mfma_f32_16x16x32_bf16 v[54:57], v[150:153], v[196:199], v[54:57]
	v_mfma_f32_16x16x32_bf16 v[46:49], v[158:161], v[196:199], v[46:49]
	v_mfma_f32_16x16x32_bf16 v[38:41], v[150:153], v[204:207], v[38:41]
	v_mfma_f32_16x16x32_bf16 v[30:33], v[158:161], v[204:207], v[30:33]
	v_mfma_f32_16x16x32_bf16 v[22:25], v[150:153], v[212:215], v[22:25]
	v_mfma_f32_16x16x32_bf16 v[14:17], v[158:161], v[212:215], v[14:17]
	v_lshl_add_u64 v[178:179], v[182:183], 0, s[10:11]
	s_mov_b32 m0, s38
	s_nop 0
	global_load_lds_dwordx4 v[178:179], off
	s_setprio 0
	s_setprio 1
	v_mfma_f32_16x16x32_bf16 v[50:53], v[162:165], v[184:187], v[50:53]
	v_mfma_f32_16x16x32_bf16 v[42:45], v[170:173], v[184:187], v[42:45]
	v_mfma_f32_16x16x32_bf16 v[34:37], v[162:165], v[192:195], v[34:37]
	v_mfma_f32_16x16x32_bf16 v[26:29], v[170:173], v[192:195], v[26:29]
	v_mfma_f32_16x16x32_bf16 v[18:21], v[162:165], v[200:203], v[18:21]
	v_mfma_f32_16x16x32_bf16 v[10:13], v[170:173], v[200:203], v[10:13]
	v_mfma_f32_16x16x32_bf16 v[6:9], v[162:165], v[208:211], v[6:9]
	v_mfma_f32_16x16x32_bf16 v[2:5], v[170:173], v[208:211], v[2:5]
	v_lshl_add_u64 v[178:179], v[216:217], 0, s[10:11]
	s_mov_b32 m0, s39
	s_nop 0
	global_load_lds_dwordx4 v[178:179], off
	v_mfma_f32_16x16x32_bf16 v[50:53], v[166:169], v[188:191], v[50:53]
	v_mfma_f32_16x16x32_bf16 v[42:45], v[174:177], v[188:191], v[42:45]
	v_mfma_f32_16x16x32_bf16 v[34:37], v[166:169], v[196:199], v[34:37]
	v_mfma_f32_16x16x32_bf16 v[26:29], v[174:177], v[196:199], v[26:29]
	v_mfma_f32_16x16x32_bf16 v[18:21], v[166:169], v[204:207], v[18:21]
	v_mfma_f32_16x16x32_bf16 v[10:13], v[174:177], v[204:207], v[10:13]
	v_mfma_f32_16x16x32_bf16 v[6:9], v[166:169], v[212:215], v[6:9]
	v_mfma_f32_16x16x32_bf16 v[2:5], v[174:177], v[212:215], v[2:5]
	s_setprio 0
	s_barrier
	s_add_i32 s51, s51, 2
	s_add_u32 s20, s20, 0x100
	s_addc_u32 s21, s21, 0
	s_add_u32 s49, s49, 0x100
	s_addc_u32 s50, s50, 0
	s_cmp_gt_u32 s51, 13
	s_cbranch_scc0 .LBB0_692
	s_and_b64 vcc, exec, s[8:9]
	s_cbranch_vccz .LBB0_695
	s_barrier

; #define PG8_STAGE(bufoff, gbase, voff) do { _Pragma("unroll") for (int _i = 0; _i < 2; ++_i) \
;         __builtin_amdgcn_global_load_lds((const unsigned*)((const char*)(gbase) + (voff)[_i]), (PG8_LAS unsigned*)(lds + (bufoff) + ldsw + _i * 8192), 16, 0, 0); } while (0)
; #define PG8_LDA(dst, b, h) do { _Pragma("unroll") for (int m = 0; m < 4; ++m) _Pragma("unroll") for (int k = 0; k < 2; ++k) dst[m][k] = *(const PG8_LAS bf16x8*)(lds + PG8_SA(b, h) + aoff + m * 2048 + k * 1024); } while (0)
; #define PG8_LDB(dst, b, h) do { _Pragma("unroll") for (int n = 0; n < 2; ++n) _Pragma("unroll") for (int k = 0; k < 2; ++k) dst[n][k] = *(const PG8_LAS bf16x8*)(lds + PG8_SB(b, h) + boff + n * 2048 + k * 1024); } while (0)
; #define PG8_WAIT_V(n) asm volatile("s_waitcnt vmcnt(" #n ")" ::: "memory")
; #define PG8_WAIT_L(n) asm volatile("s_waitcnt lgkmcnt(" #n ")" ::: "memory")
; #define PG8_BAR __builtin_amdgcn_s_barrier()
; template <class Epi, class Sched, bool ALIGN_EPI = false, bool SP2 = false, bool GATHER = false>
; __device__ __forceinline__ void gemm_phase(PG8_LAS unsigned char* lds, const Gemm g, const Sched& S, const Epi& E, int tid_in, const int* rowsrc = nullptr, PG8_LAS int* idx_lds = nullptr) {
;     ...
;         for (int t = 0; t < nt; t += 2) {
;             const bool last = (t == nt - 2);
;             if constexpr (GATHER) {
; #pragma unroll
;                 for (int h_ = 0; h_ < 2; ++h_) { gS[h_][0] = last ? gN[h_][0] : gA[h_][0]; gS[h_][1] = last ? gN[h_][1] : gA[h_][1]; } }
;             const char* a1 = cA + (size_t)(t + 1) * kstep;
;             const char* a2 = last ? nA : cA + (size_t)(t + 2) * kstep; const char* b2 = last ? nB : cB + (size_t)(t + 2) * kstep;
;             const char* a3 = a2 + kstep; const char* b3 = b2 + kstep;
;             if (last && has_next) S.a_ready(nxt);
;             if constexpr (SP2) {
;             PG8_LDB(B0, 0, 0); PG8_LDB(B1, 0, 1); PG8_SCHED; PG8_LDA(At, 0, 0); PG8_STAGE(PG8_SA(1, 1), a1 + hstepA, PG8_OA(1));
;             PG8_WAIT_V(8); PG8_WAIT_L(0); PG8_BAR; PG8_MMA(0, 0, At, B0); PG8_MMA(0, 1, At, B1); PG8_BAR; PG8_SCHED;
;             PG8_LDA(At, 0, 1); PG8_STAGE(PG8_SB(0, 0), b2, voffB); PG8_STAGE(PG8_SB(0, 1), b2 + hstep, voffB); PG8_STAGE(PG8_SA(0, 0), a2, PG8_OS(0));
;             PG8_WAIT_V(8); PG8_WAIT_L(0); PG8_BAR; PG8_MMA(1, 0, At, B0); PG8_MMA(1, 1, At, B1); PG8_BAR; PG8_SCHED;
.LBB0_1101:
	s_add_u32 s22, s20, 0xfffc0080
	s_addc_u32 s23, s21, -1
	s_add_i32 s58, 0, 0x10000
	s_cmp_eq_u32 s57, 12
	s_cselect_b32 s25, s9, s23
	s_cselect_b32 s24, s17, s22
	s_cselect_b32 s23, s7, s56
	s_cselect_b32 s22, s19, s55
	s_add_i32 s60, 0, 0x14000
	v_add_u32_e32 v142, s58, v184
	v_add_u32_e32 v182, s60, v184
	ds_read_b128 v[122:125], v142
	ds_read_b128 v[126:129], v142 offset:1024
	ds_read_b128 v[134:137], v142 offset:2048
	ds_read_b128 v[142:145], v142 offset:3072
	ds_read_b128 v[174:177], v182
	ds_read_b128 v[178:181], v182 offset:1024
	ds_read_b128 v[188:191], v182 offset:2048
	ds_read_b128 v[192:195], v182 offset:3072
	v_lshl_add_u64 v[182:183], s[20:21], 0, v[170:171]
	s_add_i32 m0, s39, 0xc000
	ds_read_b128 v[196:199], v186
	ds_read_b128 v[200:203], v186 offset:1024
	ds_read_b128 v[204:207], v186 offset:2048
	ds_read_b128 v[208:211], v186 offset:3072
	ds_read_b128 v[212:215], v186 offset:4096
	ds_read_b128 v[216:219], v186 offset:5120
	ds_read_b128 v[220:223], v186 offset:6144
	ds_read_b128 v[224:227], v186 offset:7168
	global_load_lds_dwordx4 v[182:183], off
	v_lshl_add_u64 v[182:183], s[20:21], 0, v[172:173]
	s_add_i32 m0, s39, 0xe000
	s_nop 0
	global_load_lds_dwordx4 v[182:183], off
	s_waitcnt vmcnt(8)
	s_waitcnt lgkmcnt(0)
	v_mfma_f32_16x16x32_bf16 v[138:141], v[122:125], v[196:199], v[138:141]
	v_mfma_f32_16x16x32_bf16 v[130:133], v[134:137], v[196:199], v[130:133]
	v_mfma_f32_16x16x32_bf16 v[118:121], v[122:125], v[204:207], v[118:121]
	s_barrier
	s_setprio 1
	s_waitcnt lgkmcnt(0)
	v_mfma_f32_16x16x32_bf16 v[106:109], v[134:137], v[204:207], v[106:109]
	v_mfma_f32_16x16x32_bf16 v[102:105], v[122:125], v[212:215], v[102:105]
	v_mfma_f32_16x16x32_bf16 v[90:93], v[134:137], v[212:215], v[90:93]
	v_mfma_f32_16x16x32_bf16 v[86:89], v[122:125], v[220:223], v[86:89]
	v_mfma_f32_16x16x32_bf16 v[74:77], v[134:137], v[220:223], v[74:77]
	v_mfma_f32_16x16x32_bf16 v[138:141], v[126:129], v[200:203], v[138:141]
	v_mfma_f32_16x16x32_bf16 v[130:133], v[142:145], v[200:203], v[130:133]
	v_mfma_f32_16x16x32_bf16 v[118:121], v[126:129], v[208:211], v[118:121]
	v_mfma_f32_16x16x32_bf16 v[106:109], v[142:145], v[208:211], v[106:109]
	v_mfma_f32_16x16x32_bf16 v[102:105], v[126:129], v[216:219], v[102:105]
	v_mfma_f32_16x16x32_bf16 v[90:93], v[142:145], v[216:219], v[90:93]
	v_mfma_f32_16x16x32_bf16 v[86:89], v[126:129], v[224:227], v[86:89]
	v_mfma_f32_16x16x32_bf16 v[74:77], v[142:145], v[224:227], v[74:77]
	s_setprio 0
	s_setprio 1
	v_mfma_f32_16x16x32_bf16 v[114:117], v[174:177], v[196:199], v[114:117]
	v_mfma_f32_16x16x32_bf16 v[110:113], v[188:191], v[196:199], v[110:113]
	v_mfma_f32_16x16x32_bf16 v[98:101], v[174:177], v[204:207], v[98:101]
	v_mfma_f32_16x16x32_bf16 v[94:97], v[188:191], v[204:207], v[94:97]
	v_mfma_f32_16x16x32_bf16 v[82:85], v[174:177], v[212:215], v[82:85]
	v_mfma_f32_16x16x32_bf16 v[78:81], v[188:191], v[212:215], v[78:81]
	v_mfma_f32_16x16x32_bf16 v[70:73], v[174:177], v[220:223], v[70:73]
	v_mfma_f32_16x16x32_bf16 v[66:69], v[188:191], v[220:223], v[66:69]
	v_mfma_f32_16x16x32_bf16 v[114:117], v[178:181], v[200:203], v[114:117]
	v_mfma_f32_16x16x32_bf16 v[110:113], v[192:195], v[200:203], v[110:113]
	v_mfma_f32_16x16x32_bf16 v[98:101], v[178:181], v[208:211], v[98:101]
	v_mfma_f32_16x16x32_bf16 v[94:97], v[192:195], v[208:211], v[94:97]
	v_mfma_f32_16x16x32_bf16 v[82:85], v[178:181], v[216:219], v[82:85]
	v_mfma_f32_16x16x32_bf16 v[78:81], v[192:195], v[216:219], v[78:81]
	v_mfma_f32_16x16x32_bf16 v[70:73], v[178:181], v[224:227], v[70:73]
	v_mfma_f32_16x16x32_bf16 v[66:69], v[192:195], v[224:227], v[66:69]
	s_setprio 0
	s_barrier
	s_add_i32 s58, s58, s38
	v_lshl_add_u64 v[182:183], s[22:23], 0, v[0:1]
	s_mov_b32 m0, s58
	ds_read_b128 v[196:199], v186 offset:16384
	ds_read_b128 v[200:203], v186 offset:17408
	ds_read_b128 v[204:207], v186 offset:18432
	ds_read_b128 v[208:211], v186 offset:19456
	ds_read_b128 v[212:215], v186 offset:20480
	ds_read_b128 v[216:219], v186 offset:21504
	ds_read_b128 v[220:223], v186 offset:22528
	ds_read_b128 v[224:227], v186 offset:23552
	global_load_lds_dwordx4 v[182:183], off
	s_add_i32 m0, s58, 0x2000
	s_add_u32 s58, s22, 0x40000
	v_lshl_add_u64 v[228:229], s[22:23], 0, v[148:149]
	s_addc_u32 s59, s23, 0
	s_add_i32 s60, s60, s38
	global_load_lds_dwordx4 v[228:229], off
	v_lshl_add_u64 v[230:231], s[58:59], 0, v[0:1]
	s_mov_b32 m0, s60
	v_lshl_add_u64 v[232:233], s[24:25], 0, v[150:151]
	global_load_lds_dwordx4 v[230:231], off
	s_waitcnt vmcnt(5)
	s_waitcnt lgkmcnt(0)
	v_mfma_f32_16x16x32_bf16 v[62:65], v[122:125], v[196:199], v[62:65]
	v_mfma_f32_16x16x32_bf16 v[58:61], v[134:137], v[196:199], v[58:61]
	v_mfma_f32_16x16x32_bf16 v[54:57], v[122:125], v[204:207], v[54:57]
	s_barrier
; #define PG8_STAGE(bufoff, gbase, voff) do { _Pragma("unroll") for (int _i = 0; _i < 2; ++_i) \
;         __builtin_amdgcn_global_load_lds((const unsigned*)((const char*)(gbase) + (voff)[_i]), (PG8_LAS unsigned*)(lds + (bufoff) + ldsw + _i * 8192), 16, 0, 0); } while (0)
; #define PG8_LDA(dst, b, h) do { _Pragma("unroll") for (int m = 0; m < 4; ++m) _Pragma("unroll") for (int k = 0; k < 2; ++k) dst[m][k] = *(const PG8_LAS bf16x8*)(lds + PG8_SA(b, h) + aoff + m * 2048 + k * 1024); } while (0)
; #define PG8_LDB(dst, b, h) do { _Pragma("unroll") for (int n = 0; n < 2; ++n) _Pragma("unroll") for (int k = 0; k < 2; ++k) dst[n][k] = *(const PG8_LAS bf16x8*)(lds + PG8_SB(b, h) + boff + n * 2048 + k * 1024); } while (0)
; #define PG8_MMA(ai, bj, At, Bt) do { __builtin_amdgcn_s_setprio(1); _Pragma("unroll") for (int m = 0; m < 4; ++m) _Pragma("unroll") for (int n = 0; n < 2; ++n) _Pragma("unroll") for (int k = 0; k < 2; ++k) \
;         acc[ai][bj][m][n] = __builtin_amdgcn_mfma_f32_16x16x32_bf16(Bt[n][k], At[m][k], acc[ai][bj][m][n], 0, 0, 0); __builtin_amdgcn_s_setprio(0); } while (0)
; #define PG8_WAIT_V(n) asm volatile("s_waitcnt vmcnt(" #n ")" ::: "memory")
; #define PG8_WAIT_L(n) asm volatile("s_waitcnt lgkmcnt(" #n ")" ::: "memory")
; #define PG8_BAR __builtin_amdgcn_s_barrier()
; #define PG8_SCHED __builtin_amdgcn_sched_barrier(0)
; template <class Epi, class Sched, bool ALIGN_EPI = false, bool SP2 = false, bool GATHER = false>
; __device__ __forceinline__ void gemm_phase(PG8_LAS unsigned char* lds, const Gemm g, const Sched& S, const Epi& E, int tid_in, const int* rowsrc = nullptr, PG8_LAS int* idx_lds = nullptr) {
;     ...
;             PG8_WAIT_V(8); PG8_WAIT_L(0); PG8_BAR; PG8_MMA(1, 0, At, B0); PG8_MMA(1, 1, At, B1); PG8_BAR; PG8_SCHED;
;             PG8_LDB(B0, 1, 0); PG8_LDB(B1, 1, 1); PG8_SCHED; PG8_LDA(At, 1, 0); PG8_STAGE(PG8_SA(0, 1), a2 + hstepA, PG8_OS(1));
;             PG8_WAIT_V(8); PG8_WAIT_L(0); PG8_BAR; PG8_MMA(0, 0, At, B0); PG8_MMA(0, 1, At, B1); PG8_BAR; PG8_SCHED;
	s_setprio 1
	s_waitcnt lgkmcnt(0)
	v_mfma_f32_16x16x32_bf16 v[42:45], v[134:137], v[204:207], v[42:45]
	v_mfma_f32_16x16x32_bf16 v[38:41], v[122:125], v[212:215], v[38:41]
	v_mfma_f32_16x16x32_bf16 v[26:29], v[134:137], v[212:215], v[26:29]
	v_mfma_f32_16x16x32_bf16 v[22:25], v[122:125], v[220:223], v[22:25]
	v_mfma_f32_16x16x32_bf16 v[10:13], v[134:137], v[220:223], v[10:13]
	v_lshl_add_u64 v[230:231], s[58:59], 0, v[148:149]
	s_add_i32 m0, s60, 0x2000
	s_nop 0
	global_load_lds_dwordx4 v[230:231], off
	v_mfma_f32_16x16x32_bf16 v[62:65], v[126:129], v[200:203], v[62:65]
	v_mfma_f32_16x16x32_bf16 v[58:61], v[142:145], v[200:203], v[58:61]
	v_mfma_f32_16x16x32_bf16 v[54:57], v[126:129], v[208:211], v[54:57]
	v_mfma_f32_16x16x32_bf16 v[42:45], v[142:145], v[208:211], v[42:45]
	v_mfma_f32_16x16x32_bf16 v[38:41], v[126:129], v[216:219], v[38:41]
	v_mfma_f32_16x16x32_bf16 v[26:29], v[142:145], v[216:219], v[26:29]
	v_mfma_f32_16x16x32_bf16 v[22:25], v[126:129], v[224:227], v[22:25]
	v_mfma_f32_16x16x32_bf16 v[10:13], v[142:145], v[224:227], v[10:13]
	v_lshl_add_u64 v[230:231], s[24:25], 0, v[152:153]
	s_mov_b32 m0, s39
	s_nop 0
	global_load_lds_dwordx4 v[230:231], off
	s_setprio 0
	s_setprio 1
	v_mfma_f32_16x16x32_bf16 v[50:53], v[174:177], v[196:199], v[50:53]
	v_mfma_f32_16x16x32_bf16 v[46:49], v[188:191], v[196:199], v[46:49]
	v_mfma_f32_16x16x32_bf16 v[34:37], v[174:177], v[204:207], v[34:37]
	v_mfma_f32_16x16x32_bf16 v[30:33], v[188:191], v[204:207], v[30:33]
	v_mfma_f32_16x16x32_bf16 v[18:21], v[174:177], v[212:215], v[18:21]
	v_mfma_f32_16x16x32_bf16 v[14:17], v[188:191], v[212:215], v[14:17]
	v_mfma_f32_16x16x32_bf16 v[6:9], v[174:177], v[220:223], v[6:9]
	v_mfma_f32_16x16x32_bf16 v[2:5], v[188:191], v[220:223], v[2:5]
	s_mov_b32 m0, s41
	s_nop 0
	global_load_lds_dwordx4 v[232:233], off
	v_mfma_f32_16x16x32_bf16 v[50:53], v[178:181], v[200:203], v[50:53]
	v_mfma_f32_16x16x32_bf16 v[46:49], v[192:195], v[200:203], v[46:49]
	v_mfma_f32_16x16x32_bf16 v[34:37], v[178:181], v[208:211], v[34:37]
	v_mfma_f32_16x16x32_bf16 v[30:33], v[192:195], v[208:211], v[30:33]
	v_mfma_f32_16x16x32_bf16 v[18:21], v[178:181], v[216:219], v[18:21]
	v_mfma_f32_16x16x32_bf16 v[14:17], v[192:195], v[216:219], v[14:17]
	v_mfma_f32_16x16x32_bf16 v[6:9], v[178:181], v[224:227], v[6:9]
	v_mfma_f32_16x16x32_bf16 v[2:5], v[192:195], v[224:227], v[2:5]
	s_setprio 0
	s_barrier
	s_add_i32 s58, 0, 0x18000
	s_add_i32 s59, 0, 0x1c000
	v_add_u32_e32 v142, s58, v184
	v_add_u32_e32 v187, s59, v184
	ds_read_b128 v[122:125], v142
	ds_read_b128 v[126:129], v142 offset:1024
	ds_read_b128 v[134:137], v142 offset:2048
	ds_read_b128 v[142:145], v142 offset:3072
	ds_read_b128 v[174:177], v187
	ds_read_b128 v[178:181], v187 offset:1024
	ds_read_b128 v[188:191], v187 offset:2048
	ds_read_b128 v[192:195], v187 offset:3072
	s_add_u32 s24, s24, 0x40000
	s_addc_u32 s25, s25, 0
	s_mov_b32 m0, s43
	v_lshl_add_u64 v[234:235], s[24:25], 0, v[152:153]
	ds_read_b128 v[196:199], v186 offset:32768
	ds_read_b128 v[200:203], v186 offset:33792
	ds_read_b128 v[204:207], v186 offset:34816
	ds_read_b128 v[208:211], v186 offset:35840
	ds_read_b128 v[212:215], v186 offset:36864
	ds_read_b128 v[216:219], v186 offset:37888
	ds_read_b128 v[220:223], v186 offset:38912
	ds_read_b128 v[224:227], v186 offset:39936
	global_load_lds_dwordx4 v[234:235], off
	v_lshl_add_u64 v[234:235], s[24:25], 0, v[150:151]
	s_mov_b32 m0, s45
	s_nop 0
	global_load_lds_dwordx4 v[234:235], off
	s_waitcnt vmcnt(8)
	s_waitcnt lgkmcnt(0)
	v_mfma_f32_16x16x32_bf16 v[138:141], v[122:125], v[196:199], v[138:141]
	v_mfma_f32_16x16x32_bf16 v[130:133], v[134:137], v[196:199], v[130:133]
	v_mfma_f32_16x16x32_bf16 v[118:121], v[122:125], v[204:207], v[118:121]
	s_barrier
	s_setprio 1
	s_waitcnt lgkmcnt(0)
	v_mfma_f32_16x16x32_bf16 v[106:109], v[134:137], v[204:207], v[106:109]
	v_mfma_f32_16x16x32_bf16 v[102:105], v[122:125], v[212:215], v[102:105]
	v_mfma_f32_16x16x32_bf16 v[90:93], v[134:137], v[212:215], v[90:93]
	v_mfma_f32_16x16x32_bf16 v[86:89], v[122:125], v[220:223], v[86:89]
	v_mfma_f32_16x16x32_bf16 v[74:77], v[134:137], v[220:223], v[74:77]
	v_mfma_f32_16x16x32_bf16 v[138:141], v[126:129], v[200:203], v[138:141]
	v_mfma_f32_16x16x32_bf16 v[130:133], v[142:145], v[200:203], v[130:133]
	v_mfma_f32_16x16x32_bf16 v[118:121], v[126:129], v[208:211], v[118:121]
	v_mfma_f32_16x16x32_bf16 v[106:109], v[142:145], v[208:211], v[106:109]
	v_mfma_f32_16x16x32_bf16 v[102:105], v[126:129], v[216:219], v[102:105]
	v_mfma_f32_16x16x32_bf16 v[90:93], v[142:145], v[216:219], v[90:93]
	v_mfma_f32_16x16x32_bf16 v[86:89], v[126:129], v[224:227], v[86:89]
	v_mfma_f32_16x16x32_bf16 v[74:77], v[142:145], v[224:227], v[74:77]
	s_setprio 0
	s_setprio 1
	v_mfma_f32_16x16x32_bf16 v[114:117], v[174:177], v[196:199], v[114:117]
	v_mfma_f32_16x16x32_bf16 v[110:113], v[188:191], v[196:199], v[110:113]
	v_mfma_f32_16x16x32_bf16 v[98:101], v[174:177], v[204:207], v[98:101]
	v_mfma_f32_16x16x32_bf16 v[94:97], v[188:191], v[204:207], v[94:97]
	v_mfma_f32_16x16x32_bf16 v[82:85], v[174:177], v[212:215], v[82:85]
	v_mfma_f32_16x16x32_bf16 v[78:81], v[188:191], v[212:215], v[78:81]
	v_mfma_f32_16x16x32_bf16 v[70:73], v[174:177], v[220:223], v[70:73]
	v_mfma_f32_16x16x32_bf16 v[66:69], v[188:191], v[220:223], v[66:69]
	v_mfma_f32_16x16x32_bf16 v[114:117], v[178:181], v[200:203], v[114:117]
	v_mfma_f32_16x16x32_bf16 v[110:113], v[192:195], v[200:203], v[110:113]
	v_mfma_f32_16x16x32_bf16 v[98:101], v[178:181], v[208:211], v[98:101]
	v_mfma_f32_16x16x32_bf16 v[94:97], v[192:195], v[208:211], v[94:97]
	v_mfma_f32_16x16x32_bf16 v[82:85], v[178:181], v[216:219], v[82:85]
	v_mfma_f32_16x16x32_bf16 v[78:81], v[192:195], v[216:219], v[78:81]
	v_mfma_f32_16x16x32_bf16 v[70:73], v[178:181], v[224:227], v[70:73]
	v_mfma_f32_16x16x32_bf16 v[66:69], v[192:195], v[224:227], v[66:69]
	s_setprio 0
	s_barrier
; #define PG8_STAGE(bufoff, gbase, voff) do { _Pragma("unroll") for (int _i = 0; _i < 2; ++_i) \
;         __builtin_amdgcn_global_load_lds((const unsigned*)((const char*)(gbase) + (voff)[_i]), (PG8_LAS unsigned*)(lds + (bufoff) + ldsw + _i * 8192), 16, 0, 0); } while (0)
; #define PG8_LDA(dst, b, h) do { _Pragma("unroll") for (int m = 0; m < 4; ++m) _Pragma("unroll") for (int k = 0; k < 2; ++k) dst[m][k] = *(const PG8_LAS bf16x8*)(lds + PG8_SA(b, h) + aoff + m * 2048 + k * 1024); } while (0)
; #define PG8_MMA(ai, bj, At, Bt) do { __builtin_amdgcn_s_setprio(1); _Pragma("unroll") for (int m = 0; m < 4; ++m) _Pragma("unroll") for (int n = 0; n < 2; ++n) _Pragma("unroll") for (int k = 0; k < 2; ++k) \
;         acc[ai][bj][m][n] = __builtin_amdgcn_mfma_f32_16x16x32_bf16(Bt[n][k], At[m][k], acc[ai][bj][m][n], 0, 0, 0); __builtin_amdgcn_s_setprio(0); } while (0)
; #define PG8_WAIT_V(n) asm volatile("s_waitcnt vmcnt(" #n ")" ::: "memory")
; #define PG8_WAIT_L(n) asm volatile("s_waitcnt lgkmcnt(" #n ")" ::: "memory")
; #define PG8_BAR __builtin_amdgcn_s_barrier()
; #define PG8_SCHED __builtin_amdgcn_sched_barrier(0)
; template <class Epi, class Sched, bool ALIGN_EPI = false, bool SP2 = false, bool GATHER = false>
; __device__ __forceinline__ void gemm_phase(PG8_LAS unsigned char* lds, const Gemm g, const Sched& S, const Epi& E, int tid_in, const int* rowsrc = nullptr, PG8_LAS int* idx_lds = nullptr) {
;     ...
;             PG8_LDA(At, 1, 1); PG8_STAGE(PG8_SB(1, 0), b3, voffB); PG8_STAGE(PG8_SB(1, 1), b3 + hstep, voffB); PG8_STAGE(PG8_SA(1, 0), a3, PG8_OS(0));
;             PG8_WAIT_V(8); PG8_WAIT_L(0); PG8_BAR; PG8_MMA(1, 0, At, B0); PG8_MMA(1, 1, At, B1); PG8_BAR; PG8_SCHED;
;     ...
;         if constexpr (ALIGN_EPI) { if (wr == 0) PG8_BAR; }
	s_add_i32 s24, s58, s38
	v_lshl_add_u64 v[182:183], v[182:183], 0, s[10:11]
	s_mov_b32 m0, s24
	ds_read_b128 v[196:199], v186 offset:49152
	ds_read_b128 v[200:203], v186 offset:50176
	ds_read_b128 v[204:207], v186 offset:51200
	ds_read_b128 v[208:211], v186 offset:52224
	ds_read_b128 v[212:215], v186 offset:53248
	ds_read_b128 v[216:219], v186 offset:54272
	ds_read_b128 v[220:223], v186 offset:55296
	ds_read_b128 v[224:227], v186 offset:56320
	global_load_lds_dwordx4 v[182:183], off
	s_add_i32 m0, s24, 0x2000
	s_add_u32 s22, s22, 0x40080
	v_lshl_add_u64 v[182:183], v[228:229], 0, s[10:11]
	s_addc_u32 s23, s23, 0
	s_add_i32 s24, s59, s38
	global_load_lds_dwordx4 v[182:183], off
	v_lshl_add_u64 v[182:183], s[22:23], 0, v[0:1]
	s_mov_b32 m0, s24
	s_nop 0
	global_load_lds_dwordx4 v[182:183], off
	s_waitcnt vmcnt(5)
	s_waitcnt lgkmcnt(0)
	v_mfma_f32_16x16x32_bf16 v[62:65], v[122:125], v[196:199], v[62:65]
	v_mfma_f32_16x16x32_bf16 v[58:61], v[134:137], v[196:199], v[58:61]
	v_mfma_f32_16x16x32_bf16 v[54:57], v[122:125], v[204:207], v[54:57]
	s_barrier
	s_setprio 1
	s_waitcnt lgkmcnt(0)
	v_mfma_f32_16x16x32_bf16 v[42:45], v[134:137], v[204:207], v[42:45]
	v_mfma_f32_16x16x32_bf16 v[38:41], v[122:125], v[212:215], v[38:41]
	v_mfma_f32_16x16x32_bf16 v[26:29], v[134:137], v[212:215], v[26:29]
	v_mfma_f32_16x16x32_bf16 v[22:25], v[122:125], v[220:223], v[22:25]
	v_mfma_f32_16x16x32_bf16 v[10:13], v[134:137], v[220:223], v[10:13]
	v_lshl_add_u64 v[182:183], s[22:23], 0, v[148:149]
	s_add_i32 m0, s24, 0x2000
	s_nop 0
	global_load_lds_dwordx4 v[182:183], off
	v_mfma_f32_16x16x32_bf16 v[62:65], v[126:129], v[200:203], v[62:65]
	v_mfma_f32_16x16x32_bf16 v[58:61], v[142:145], v[200:203], v[58:61]
	v_mfma_f32_16x16x32_bf16 v[54:57], v[126:129], v[208:211], v[54:57]
	v_mfma_f32_16x16x32_bf16 v[42:45], v[142:145], v[208:211], v[42:45]
	v_mfma_f32_16x16x32_bf16 v[38:41], v[126:129], v[216:219], v[38:41]
	v_mfma_f32_16x16x32_bf16 v[26:29], v[142:145], v[216:219], v[26:29]
	v_mfma_f32_16x16x32_bf16 v[22:25], v[126:129], v[224:227], v[22:25]
	v_mfma_f32_16x16x32_bf16 v[10:13], v[142:145], v[224:227], v[10:13]
	v_lshl_add_u64 v[182:183], v[230:231], 0, s[10:11]
	s_mov_b32 m0, s52
	s_nop 0
	global_load_lds_dwordx4 v[182:183], off
	s_setprio 0
	s_setprio 1
	v_mfma_f32_16x16x32_bf16 v[50:53], v[174:177], v[196:199], v[50:53]
	v_mfma_f32_16x16x32_bf16 v[46:49], v[188:191], v[196:199], v[46:49]
	v_mfma_f32_16x16x32_bf16 v[34:37], v[174:177], v[204:207], v[34:37]
	v_mfma_f32_16x16x32_bf16 v[30:33], v[188:191], v[204:207], v[30:33]
	v_mfma_f32_16x16x32_bf16 v[18:21], v[174:177], v[212:215], v[18:21]
	v_mfma_f32_16x16x32_bf16 v[14:17], v[188:191], v[212:215], v[14:17]
	v_mfma_f32_16x16x32_bf16 v[6:9], v[174:177], v[220:223], v[6:9]
	v_mfma_f32_16x16x32_bf16 v[2:5], v[188:191], v[220:223], v[2:5]
	v_lshl_add_u64 v[182:183], v[232:233], 0, s[10:11]
	s_mov_b32 m0, s53
	s_nop 0
	global_load_lds_dwordx4 v[182:183], off
	v_mfma_f32_16x16x32_bf16 v[50:53], v[178:181], v[200:203], v[50:53]
	v_mfma_f32_16x16x32_bf16 v[46:49], v[192:195], v[200:203], v[46:49]
	v_mfma_f32_16x16x32_bf16 v[34:37], v[178:181], v[208:211], v[34:37]
	v_mfma_f32_16x16x32_bf16 v[30:33], v[192:195], v[208:211], v[30:33]
	v_mfma_f32_16x16x32_bf16 v[18:21], v[178:181], v[216:219], v[18:21]
	v_mfma_f32_16x16x32_bf16 v[14:17], v[192:195], v[216:219], v[14:17]
	v_mfma_f32_16x16x32_bf16 v[6:9], v[178:181], v[224:227], v[6:9]
	v_mfma_f32_16x16x32_bf16 v[2:5], v[192:195], v[224:227], v[2:5]
	s_setprio 0
	s_barrier
	s_add_i32 s57, s57, 2
	s_add_u32 s20, s20, 0x100
	s_addc_u32 s21, s21, 0
	s_add_u32 s55, s55, 0x100
	s_addc_u32 s56, s56, 0
	s_cmp_gt_u32 s57, 13
	s_cbranch_scc0 .LBB0_1101
	s_and_b64 vcc, exec, s[4:5]
	s_cbranch_vccz .LBB0_1104
	s_barrier

;     ...
;     if (FFN) {
;         const float* R = A[I_ROUTER] + (size_t)layer * 1024 * 16;
;         for (int i = F.tid; i < 16 * 1024; i += NTHREADS) { const int k = i >> 4, e = i & 15; rT[e * 1024 + (k & 512) + ((k >> 2) & 1) * 256 + ((k >> 3) & 63) * 4 + (k & 3)] = R[i]; }
;         __syncthreads();
.LBB0_1683:
	s_andn2_b64 vcc, exec, s[0:1]
	s_cbranch_vccnz .LBB0_1776
	v_readlane_b32 s0, v251, 12
	v_mbcnt_lo_u32_b32 v0, -1, 0
	v_mbcnt_hi_u32_b32 v0, -1, v0
	s_mov_b64 s[8:9], 0
	v_readlane_b32 s21, v251, 2
	v_add_u32_e32 v46, s0, v0
	v_readlane_b32 s0, v252, 32
	v_readlane_b32 s1, v252, 33
	s_mov_b32 s1, s3
	v_writelane_b32 v252, s0, 32
	v_readlane_b32 s16, v251, 3
	v_readfirstlane_b32 s2, v46
	v_writelane_b32 v252, s1, 33
	s_movk_i32 s0, 0x4000
	v_cmp_gt_i32_e32 vcc, s0, v46
	v_readlane_b32 s0, v252, 25
	s_nop 1
	v_mov_b32_e32 v0, s0
	ds_read_b32 v0, v0
	v_readlane_b32 s0, v252, 26
	s_waitcnt lgkmcnt(0)
	v_readfirstlane_b32 s17, v0
	v_mov_b32_e32 v0, s0
	ds_read_b32 v0, v0
	s_waitcnt lgkmcnt(0)
	v_readfirstlane_b32 s18, v0
	s_and_saveexec_b64 s[0:1], vcc
	s_cbranch_execz .LBB0_1696
	s_waitcnt vmcnt(0)
	v_readlane_b32 s6, v252, 32
	v_readlane_b32 s7, v252, 33
	s_lshl_b64 s[6:7], s[6:7], 16
	s_add_u32 s6, s17, s6
	s_addc_u32 s7, s18, s7
	v_and_b32_e32 v2, 15, v46
	v_lshrrev_b32_e32 v3, 4, v46
	v_lshlrev_b32_e32 v4, 12, v2
	v_bfe_u32 v5, v3, 2, 1
	v_lshl_or_b32 v4, v5, 10, v4
	v_lshrrev_b32_e32 v5, 3, v3
	v_lshl_or_b32 v4, v5, 4, v4
	v_and_b32_e32 v5, 3, v3
	v_lshl_or_b32 v4, v5, 2, v4
	v_lshlrev_b32_e32 v5, 2, v46
	v_add_u32_e32 v6, 0x1000, v5
	v_add_u32_e32 v7, 0x2000, v5
	v_add_u32_e32 v8, 0x3000, v5
	v_add_u32_e32 v9, 0x4000, v5
	v_add_u32_e32 v10, 0x5000, v5
	v_add_u32_e32 v11, 0x6000, v5
	v_add_u32_e32 v12, 0x7000, v5
	global_load_dword v154, v5, s[6:7]
	global_load_dword v155, v5, s[6:7] offset:2048
	global_load_dword v156, v6, s[6:7]
	global_load_dword v157, v6, s[6:7] offset:2048
	global_load_dword v158, v7, s[6:7]
	global_load_dword v159, v7, s[6:7] offset:2048
	global_load_dword v160, v8, s[6:7]
	global_load_dword v161, v8, s[6:7] offset:2048
	global_load_dword v162, v9, s[6:7]
	global_load_dword v163, v9, s[6:7] offset:2048
	global_load_dword v164, v10, s[6:7]
	global_load_dword v165, v10, s[6:7] offset:2048
	global_load_dword v166, v11, s[6:7]
	global_load_dword v167, v11, s[6:7] offset:2048
	global_load_dword v168, v12, s[6:7]
	global_load_dword v169, v12, s[6:7] offset:2048
	s_waitcnt vmcnt(0)
	ds_write_b32 v4, v154
	ds_write_b32 v4, v155 offset:64
	ds_write_b32 v4, v156 offset:128
	ds_write_b32 v4, v157 offset:192
	ds_write_b32 v4, v158 offset:256
	ds_write_b32 v4, v159 offset:320
	ds_write_b32 v4, v160 offset:384
	ds_write_b32 v4, v161 offset:448
	ds_write_b32 v4, v162 offset:512
	ds_write_b32 v4, v163 offset:576
	ds_write_b32 v4, v164 offset:640
	ds_write_b32 v4, v165 offset:704
	ds_write_b32 v4, v166 offset:768
	ds_write_b32 v4, v167 offset:832
	ds_write_b32 v4, v168 offset:896
	ds_write_b32 v4, v169 offset:960
	v_add_u32_e32 v5, 0x8000, v5
	v_add_u32_e32 v6, 0x8000, v6
	v_add_u32_e32 v7, 0x8000, v7
	v_add_u32_e32 v8, 0x8000, v8
	v_add_u32_e32 v9, 0x8000, v9
	v_add_u32_e32 v10, 0x8000, v10
	v_add_u32_e32 v11, 0x8000, v11
	v_add_u32_e32 v12, 0x8000, v12
	global_load_dword v154, v5, s[6:7]
	global_load_dword v155, v5, s[6:7] offset:2048
	global_load_dword v156, v6, s[6:7]
	global_load_dword v157, v6, s[6:7] offset:2048
	global_load_dword v158, v7, s[6:7]
	global_load_dword v159, v7, s[6:7] offset:2048
	global_load_dword v160, v8, s[6:7]
	global_load_dword v161, v8, s[6:7] offset:2048
	global_load_dword v162, v9, s[6:7]
	global_load_dword v163, v9, s[6:7] offset:2048
	global_load_dword v164, v10, s[6:7]
	global_load_dword v165, v10, s[6:7] offset:2048
	global_load_dword v166, v11, s[6:7]
	global_load_dword v167, v11, s[6:7] offset:2048
	global_load_dword v168, v12, s[6:7]
	global_load_dword v169, v12, s[6:7] offset:2048
	s_waitcnt vmcnt(0)
	ds_write_b32 v4, v154 offset:2048
	ds_write_b32 v4, v155 offset:2112
	ds_write_b32 v4, v156 offset:2176
	ds_write_b32 v4, v157 offset:2240
	ds_write_b32 v4, v158 offset:2304
	ds_write_b32 v4, v159 offset:2368
	ds_write_b32 v4, v160 offset:2432
	ds_write_b32 v4, v161 offset:2496
	ds_write_b32 v4, v162 offset:2560
	ds_write_b32 v4, v163 offset:2624
	ds_write_b32 v4, v164 offset:2688
	ds_write_b32 v4, v165 offset:2752
	ds_write_b32 v4, v166 offset:2816
	ds_write_b32 v4, v167 offset:2880
	ds_write_b32 v4, v168 offset:2944
	ds_write_b32 v4, v169 offset:3008

; #define PG8_STAGE(bufoff, gbase, voff) do { _Pragma("unroll") for (int _i = 0; _i < 2; ++_i) \
;         __builtin_amdgcn_global_load_lds((const unsigned*)((const char*)(gbase) + (voff)[_i]), (PG8_LAS unsigned*)(lds + (bufoff) + ldsw + _i * 8192), 16, 0, 0); } while (0)
; #define PG8_LDA(dst, b, h) do { _Pragma("unroll") for (int m = 0; m < 4; ++m) _Pragma("unroll") for (int k = 0; k < 2; ++k) dst[m][k] = *(const PG8_LAS bf16x8*)(lds + PG8_SA(b, h) + aoff + m * 2048 + k * 1024); } while (0)
; #define PG8_LDB(dst, b, h) do { _Pragma("unroll") for (int n = 0; n < 2; ++n) _Pragma("unroll") for (int k = 0; k < 2; ++k) dst[n][k] = *(const PG8_LAS bf16x8*)(lds + PG8_SB(b, h) + boff + n * 2048 + k * 1024); } while (0)
; #define PG8_WAIT_V(n) asm volatile("s_waitcnt vmcnt(" #n ")" ::: "memory")
; #define PG8_WAIT_L(n) asm volatile("s_waitcnt lgkmcnt(" #n ")" ::: "memory")
; #define PG8_BAR __builtin_amdgcn_s_barrier()
; #define PG8_SCHED __builtin_amdgcn_sched_barrier(0)
; template <class Epi, class Sched, bool ALIGN_EPI = false, bool SP2 = false, bool GATHER = false>
; __device__ __forceinline__ void gemm_phase(PG8_LAS unsigned char* lds, const Gemm g, const Sched& S, const Epi& E, int tid_in, const int* rowsrc = nullptr, PG8_LAS int* idx_lds = nullptr) {
;     ...
;         for (int t = 0; t < nt; t += 2) {
;             const bool last = (t == nt - 2);
;             if constexpr (GATHER) {
; #pragma unroll
;                 for (int h_ = 0; h_ < 2; ++h_) { gS[h_][0] = last ? gN[h_][0] : gA[h_][0]; gS[h_][1] = last ? gN[h_][1] : gA[h_][1]; } }
;             const char* a1 = cA + (size_t)(t + 1) * kstep;
;             const char* a2 = last ? nA : cA + (size_t)(t + 2) * kstep; const char* b2 = last ? nB : cB + (size_t)(t + 2) * kstep;
;             const char* a3 = a2 + kstep; const char* b3 = b2 + kstep;
;             if (last && has_next) S.a_ready(nxt);
;             if constexpr (SP2) {
;             PG8_LDB(B0, 0, 0); PG8_LDB(B1, 0, 1); PG8_SCHED; PG8_LDA(At, 0, 0); PG8_STAGE(PG8_SA(1, 1), a1 + hstepA, PG8_OA(1));
;             PG8_WAIT_V(8); PG8_WAIT_L(0); PG8_BAR; PG8_MMA(0, 0, At, B0); PG8_MMA(0, 1, At, B1); PG8_BAR; PG8_SCHED;
;             PG8_LDA(At, 0, 1); PG8_STAGE(PG8_SB(0, 0), b2, voffB); PG8_STAGE(PG8_SB(0, 1), b2 + hstep, voffB); PG8_STAGE(PG8_SA(0, 0), a2, PG8_OS(0));
.LBB0_2005:
	s_add_u32 s28, s26, 0xfffc0080
	s_addc_u32 s29, s27, -1
	s_add_i32 s58, 0, 0x10000
	s_cmp_eq_u32 s57, 12
	s_cselect_b32 s31, s13, s29
	s_cselect_b32 s30, s23, s28
	v_add_u32_e32 v0, s58, v151
	s_cselect_b32 s29, s15, s56
	s_cselect_b32 s28, s43, s55
	s_add_i32 s60, 0, 0x14000
	ds_read_b128 v[142:145], v0
	ds_read_b128 v[154:157], v0 offset:1024
	ds_read_b128 v[158:161], v0 offset:2048
	ds_read_b128 v[162:165], v0 offset:3072
	v_add_u32_e32 v0, s60, v151
	ds_read_b128 v[166:169], v0
	ds_read_b128 v[170:173], v0 offset:1024
	ds_read_b128 v[174:177], v0 offset:2048
	ds_read_b128 v[178:181], v0 offset:3072
	v_lshl_add_u64 v[148:149], s[26:27], 0, v[138:139]
	s_add_i32 m0, s25, 0xc000
	ds_read_b128 v[182:185], v153
	ds_read_b128 v[186:189], v153 offset:1024
	ds_read_b128 v[190:193], v153 offset:2048
	ds_read_b128 v[194:197], v153 offset:3072
	ds_read_b128 v[198:201], v153 offset:4096
	ds_read_b128 v[202:205], v153 offset:5120
	ds_read_b128 v[206:209], v153 offset:6144
	ds_read_b128 v[210:213], v153 offset:7168
	global_load_lds_dwordx4 v[148:149], off
	v_lshl_add_u64 v[148:149], s[26:27], 0, v[140:141]
	s_add_i32 m0, s25, 0xe000
	s_nop 0
	global_load_lds_dwordx4 v[148:149], off
	s_waitcnt vmcnt(8)
	s_waitcnt lgkmcnt(0)
	v_mfma_f32_16x16x32_bf16 v[126:129], v[142:145], v[182:185], v[126:129]
	v_mfma_f32_16x16x32_bf16 v[122:125], v[158:161], v[182:185], v[122:125]
	v_mfma_f32_16x16x32_bf16 v[110:113], v[142:145], v[190:193], v[110:113]
	s_barrier
	s_setprio 1
	s_waitcnt lgkmcnt(0)
	v_mfma_f32_16x16x32_bf16 v[106:109], v[158:161], v[190:193], v[106:109]
	v_mfma_f32_16x16x32_bf16 v[94:97], v[142:145], v[198:201], v[94:97]
	v_mfma_f32_16x16x32_bf16 v[90:93], v[158:161], v[198:201], v[90:93]
	v_mfma_f32_16x16x32_bf16 v[78:81], v[142:145], v[206:209], v[78:81]
	v_mfma_f32_16x16x32_bf16 v[74:77], v[158:161], v[206:209], v[74:77]
	v_mfma_f32_16x16x32_bf16 v[126:129], v[154:157], v[186:189], v[126:129]
	v_mfma_f32_16x16x32_bf16 v[122:125], v[162:165], v[186:189], v[122:125]
	v_mfma_f32_16x16x32_bf16 v[110:113], v[154:157], v[194:197], v[110:113]
	v_mfma_f32_16x16x32_bf16 v[106:109], v[162:165], v[194:197], v[106:109]
	v_mfma_f32_16x16x32_bf16 v[94:97], v[154:157], v[202:205], v[94:97]
	v_mfma_f32_16x16x32_bf16 v[90:93], v[162:165], v[202:205], v[90:93]
	v_mfma_f32_16x16x32_bf16 v[78:81], v[154:157], v[210:213], v[78:81]
	v_mfma_f32_16x16x32_bf16 v[74:77], v[162:165], v[210:213], v[74:77]
	s_setprio 0
	s_setprio 1
	v_mfma_f32_16x16x32_bf16 v[118:121], v[166:169], v[182:185], v[118:121]
	v_mfma_f32_16x16x32_bf16 v[114:117], v[174:177], v[182:185], v[114:117]
	v_mfma_f32_16x16x32_bf16 v[102:105], v[166:169], v[190:193], v[102:105]
	v_mfma_f32_16x16x32_bf16 v[98:101], v[174:177], v[190:193], v[98:101]
	v_mfma_f32_16x16x32_bf16 v[86:89], v[166:169], v[198:201], v[86:89]
	v_mfma_f32_16x16x32_bf16 v[82:85], v[174:177], v[198:201], v[82:85]
	v_mfma_f32_16x16x32_bf16 v[70:73], v[166:169], v[206:209], v[70:73]
	v_mfma_f32_16x16x32_bf16 v[66:69], v[174:177], v[206:209], v[66:69]
	v_mfma_f32_16x16x32_bf16 v[118:121], v[170:173], v[186:189], v[118:121]
	v_mfma_f32_16x16x32_bf16 v[114:117], v[178:181], v[186:189], v[114:117]
	v_mfma_f32_16x16x32_bf16 v[102:105], v[170:173], v[194:197], v[102:105]
	v_mfma_f32_16x16x32_bf16 v[98:101], v[178:181], v[194:197], v[98:101]
	v_mfma_f32_16x16x32_bf16 v[86:89], v[170:173], v[202:205], v[86:89]
	v_mfma_f32_16x16x32_bf16 v[82:85], v[178:181], v[202:205], v[82:85]
	v_mfma_f32_16x16x32_bf16 v[70:73], v[170:173], v[210:213], v[70:73]
	v_mfma_f32_16x16x32_bf16 v[66:69], v[178:181], v[210:213], v[66:69]
	s_setprio 0
	s_barrier
	s_add_i32 s58, s58, s44
	v_lshl_add_u64 v[148:149], s[28:29], 0, v[134:135]
	s_mov_b32 m0, s58
	ds_read_b128 v[182:185], v153 offset:16384
	ds_read_b128 v[186:189], v153 offset:17408
	ds_read_b128 v[190:193], v153 offset:18432
	ds_read_b128 v[194:197], v153 offset:19456
	ds_read_b128 v[198:201], v153 offset:20480
	ds_read_b128 v[202:205], v153 offset:21504
	ds_read_b128 v[206:209], v153 offset:22528
	ds_read_b128 v[210:213], v153 offset:23552
	global_load_lds_dwordx4 v[148:149], off
	s_add_i32 m0, s58, 0x2000
	s_add_u32 s58, s28, 0x40000
	v_lshl_add_u64 v[214:215], s[28:29], 0, v[130:131]
	s_addc_u32 s59, s29, 0
	s_add_i32 s60, s60, s44
	global_load_lds_dwordx4 v[214:215], off
	v_lshl_add_u64 v[216:217], s[58:59], 0, v[134:135]
	s_mov_b32 m0, s60
	v_lshl_add_u64 v[218:219], s[30:31], 0, v[132:133]
	global_load_lds_dwordx4 v[216:217], off
	s_waitcnt vmcnt(5)
	s_waitcnt lgkmcnt(0)
	v_mfma_f32_16x16x32_bf16 v[62:65], v[142:145], v[182:185], v[62:65]
	v_mfma_f32_16x16x32_bf16 v[58:61], v[158:161], v[182:185], v[58:61]
	v_mfma_f32_16x16x32_bf16 v[46:49], v[142:145], v[190:193], v[46:49]
	s_barrier
; #define PG8_STAGE(bufoff, gbase, voff) do { _Pragma("unroll") for (int _i = 0; _i < 2; ++_i) \
;         __builtin_amdgcn_global_load_lds((const unsigned*)((const char*)(gbase) + (voff)[_i]), (PG8_LAS unsigned*)(lds + (bufoff) + ldsw + _i * 8192), 16, 0, 0); } while (0)
; #define PG8_LDA(dst, b, h) do { _Pragma("unroll") for (int m = 0; m < 4; ++m) _Pragma("unroll") for (int k = 0; k < 2; ++k) dst[m][k] = *(const PG8_LAS bf16x8*)(lds + PG8_SA(b, h) + aoff + m * 2048 + k * 1024); } while (0)
; #define PG8_LDB(dst, b, h) do { _Pragma("unroll") for (int n = 0; n < 2; ++n) _Pragma("unroll") for (int k = 0; k < 2; ++k) dst[n][k] = *(const PG8_LAS bf16x8*)(lds + PG8_SB(b, h) + boff + n * 2048 + k * 1024); } while (0)
; #define PG8_MMA(ai, bj, At, Bt) do { __builtin_amdgcn_s_setprio(1); _Pragma("unroll") for (int m = 0; m < 4; ++m) _Pragma("unroll") for (int n = 0; n < 2; ++n) _Pragma("unroll") for (int k = 0; k < 2; ++k) \
;         acc[ai][bj][m][n] = __builtin_amdgcn_mfma_f32_16x16x32_bf16(Bt[n][k], At[m][k], acc[ai][bj][m][n], 0, 0, 0); __builtin_amdgcn_s_setprio(0); } while (0)
; #define PG8_WAIT_V(n) asm volatile("s_waitcnt vmcnt(" #n ")" ::: "memory")
; #define PG8_WAIT_L(n) asm volatile("s_waitcnt lgkmcnt(" #n ")" ::: "memory")
; #define PG8_BAR __builtin_amdgcn_s_barrier()
; #define PG8_SCHED __builtin_amdgcn_sched_barrier(0)
; template <class Epi, class Sched, bool ALIGN_EPI = false, bool SP2 = false, bool GATHER = false>
; __device__ __forceinline__ void gemm_phase(PG8_LAS unsigned char* lds, const Gemm g, const Sched& S, const Epi& E, int tid_in, const int* rowsrc = nullptr, PG8_LAS int* idx_lds = nullptr) {
;     ...
;             PG8_LDA(At, 0, 1); PG8_STAGE(PG8_SB(0, 0), b2, voffB); PG8_STAGE(PG8_SB(0, 1), b2 + hstep, voffB); PG8_STAGE(PG8_SA(0, 0), a2, PG8_OS(0));
;             PG8_WAIT_V(8); PG8_WAIT_L(0); PG8_BAR; PG8_MMA(1, 0, At, B0); PG8_MMA(1, 1, At, B1); PG8_BAR; PG8_SCHED;
;             PG8_LDB(B0, 1, 0); PG8_LDB(B1, 1, 1); PG8_SCHED; PG8_LDA(At, 1, 0); PG8_STAGE(PG8_SA(0, 1), a2 + hstepA, PG8_OS(1));
;             PG8_WAIT_V(8); PG8_WAIT_L(0); PG8_BAR; PG8_MMA(0, 0, At, B0); PG8_MMA(0, 1, At, B1); PG8_BAR; PG8_SCHED;
	s_setprio 1
	s_waitcnt lgkmcnt(0)
	v_mfma_f32_16x16x32_bf16 v[42:45], v[158:161], v[190:193], v[42:45]
	v_mfma_f32_16x16x32_bf16 v[30:33], v[142:145], v[198:201], v[30:33]
	v_mfma_f32_16x16x32_bf16 v[26:29], v[158:161], v[198:201], v[26:29]
	v_mfma_f32_16x16x32_bf16 v[14:17], v[142:145], v[206:209], v[14:17]
	v_mfma_f32_16x16x32_bf16 v[10:13], v[158:161], v[206:209], v[10:13]
	v_lshl_add_u64 v[216:217], s[58:59], 0, v[130:131]
	s_add_i32 m0, s60, 0x2000
	s_nop 0
	global_load_lds_dwordx4 v[216:217], off
	v_mfma_f32_16x16x32_bf16 v[62:65], v[154:157], v[186:189], v[62:65]
	v_mfma_f32_16x16x32_bf16 v[58:61], v[162:165], v[186:189], v[58:61]
	v_mfma_f32_16x16x32_bf16 v[46:49], v[154:157], v[194:197], v[46:49]
	v_mfma_f32_16x16x32_bf16 v[42:45], v[162:165], v[194:197], v[42:45]
	v_mfma_f32_16x16x32_bf16 v[30:33], v[154:157], v[202:205], v[30:33]
	v_mfma_f32_16x16x32_bf16 v[26:29], v[162:165], v[202:205], v[26:29]
	v_mfma_f32_16x16x32_bf16 v[14:17], v[154:157], v[210:213], v[14:17]
	v_mfma_f32_16x16x32_bf16 v[10:13], v[162:165], v[210:213], v[10:13]
	v_lshl_add_u64 v[216:217], s[30:31], 0, v[136:137]
	s_mov_b32 m0, s25
	s_nop 0
	global_load_lds_dwordx4 v[216:217], off
	s_setprio 0
	s_setprio 1
	v_mfma_f32_16x16x32_bf16 v[54:57], v[166:169], v[182:185], v[54:57]
	v_mfma_f32_16x16x32_bf16 v[50:53], v[174:177], v[182:185], v[50:53]
	v_mfma_f32_16x16x32_bf16 v[38:41], v[166:169], v[190:193], v[38:41]
	v_mfma_f32_16x16x32_bf16 v[34:37], v[174:177], v[190:193], v[34:37]
	v_mfma_f32_16x16x32_bf16 v[22:25], v[166:169], v[198:201], v[22:25]
	v_mfma_f32_16x16x32_bf16 v[18:21], v[174:177], v[198:201], v[18:21]
	v_mfma_f32_16x16x32_bf16 v[6:9], v[166:169], v[206:209], v[6:9]
	v_mfma_f32_16x16x32_bf16 v[2:5], v[174:177], v[206:209], v[2:5]
	s_mov_b32 m0, s48
	s_nop 0
	global_load_lds_dwordx4 v[218:219], off
	v_mfma_f32_16x16x32_bf16 v[54:57], v[170:173], v[186:189], v[54:57]
	v_mfma_f32_16x16x32_bf16 v[50:53], v[178:181], v[186:189], v[50:53]
	v_mfma_f32_16x16x32_bf16 v[38:41], v[170:173], v[194:197], v[38:41]
	v_mfma_f32_16x16x32_bf16 v[34:37], v[178:181], v[194:197], v[34:37]
	v_mfma_f32_16x16x32_bf16 v[22:25], v[170:173], v[202:205], v[22:25]
	v_mfma_f32_16x16x32_bf16 v[18:21], v[178:181], v[202:205], v[18:21]
	v_mfma_f32_16x16x32_bf16 v[6:9], v[170:173], v[210:213], v[6:9]
	v_mfma_f32_16x16x32_bf16 v[2:5], v[178:181], v[210:213], v[2:5]
	s_setprio 0
	s_barrier
	s_add_i32 s58, 0, 0x18000
	v_add_u32_e32 v0, s58, v151
	s_add_i32 s59, 0, 0x1c000
	ds_read_b128 v[142:145], v0
	ds_read_b128 v[154:157], v0 offset:1024
	ds_read_b128 v[158:161], v0 offset:2048
	ds_read_b128 v[162:165], v0 offset:3072
	v_add_u32_e32 v0, s59, v151
	ds_read_b128 v[166:169], v0
	ds_read_b128 v[170:173], v0 offset:1024
	ds_read_b128 v[174:177], v0 offset:2048
	ds_read_b128 v[178:181], v0 offset:3072
	s_add_u32 s30, s30, 0x40000
	s_addc_u32 s31, s31, 0
	s_mov_b32 m0, s49
	v_lshl_add_u64 v[220:221], s[30:31], 0, v[136:137]
	ds_read_b128 v[182:185], v153 offset:32768
	ds_read_b128 v[186:189], v153 offset:33792
	ds_read_b128 v[190:193], v153 offset:34816
	ds_read_b128 v[194:197], v153 offset:35840
	ds_read_b128 v[198:201], v153 offset:36864
	ds_read_b128 v[202:205], v153 offset:37888
	ds_read_b128 v[206:209], v153 offset:38912
	ds_read_b128 v[210:213], v153 offset:39936
	global_load_lds_dwordx4 v[220:221], off
	v_lshl_add_u64 v[220:221], s[30:31], 0, v[132:133]
	s_mov_b32 m0, s50
	s_nop 0
	global_load_lds_dwordx4 v[220:221], off
	s_waitcnt vmcnt(8)
	s_waitcnt lgkmcnt(0)
	v_mfma_f32_16x16x32_bf16 v[126:129], v[142:145], v[182:185], v[126:129]
	v_mfma_f32_16x16x32_bf16 v[122:125], v[158:161], v[182:185], v[122:125]
	v_mfma_f32_16x16x32_bf16 v[110:113], v[142:145], v[190:193], v[110:113]
	s_barrier
	s_setprio 1
	s_waitcnt lgkmcnt(0)
	v_mfma_f32_16x16x32_bf16 v[106:109], v[158:161], v[190:193], v[106:109]
	v_mfma_f32_16x16x32_bf16 v[94:97], v[142:145], v[198:201], v[94:97]
	v_mfma_f32_16x16x32_bf16 v[90:93], v[158:161], v[198:201], v[90:93]
	v_mfma_f32_16x16x32_bf16 v[78:81], v[142:145], v[206:209], v[78:81]
	v_mfma_f32_16x16x32_bf16 v[74:77], v[158:161], v[206:209], v[74:77]
	v_mfma_f32_16x16x32_bf16 v[126:129], v[154:157], v[186:189], v[126:129]
	v_mfma_f32_16x16x32_bf16 v[122:125], v[162:165], v[186:189], v[122:125]
	v_mfma_f32_16x16x32_bf16 v[110:113], v[154:157], v[194:197], v[110:113]
	v_mfma_f32_16x16x32_bf16 v[106:109], v[162:165], v[194:197], v[106:109]
	v_mfma_f32_16x16x32_bf16 v[94:97], v[154:157], v[202:205], v[94:97]
	v_mfma_f32_16x16x32_bf16 v[90:93], v[162:165], v[202:205], v[90:93]
	v_mfma_f32_16x16x32_bf16 v[78:81], v[154:157], v[210:213], v[78:81]
	v_mfma_f32_16x16x32_bf16 v[74:77], v[162:165], v[210:213], v[74:77]
	s_setprio 0
	s_setprio 1
	v_mfma_f32_16x16x32_bf16 v[118:121], v[166:169], v[182:185], v[118:121]
	v_mfma_f32_16x16x32_bf16 v[114:117], v[174:177], v[182:185], v[114:117]
	v_mfma_f32_16x16x32_bf16 v[102:105], v[166:169], v[190:193], v[102:105]
	v_mfma_f32_16x16x32_bf16 v[98:101], v[174:177], v[190:193], v[98:101]
	v_mfma_f32_16x16x32_bf16 v[86:89], v[166:169], v[198:201], v[86:89]
	v_mfma_f32_16x16x32_bf16 v[82:85], v[174:177], v[198:201], v[82:85]
	v_mfma_f32_16x16x32_bf16 v[70:73], v[166:169], v[206:209], v[70:73]
	v_mfma_f32_16x16x32_bf16 v[66:69], v[174:177], v[206:209], v[66:69]
	v_mfma_f32_16x16x32_bf16 v[118:121], v[170:173], v[186:189], v[118:121]
	v_mfma_f32_16x16x32_bf16 v[114:117], v[178:181], v[186:189], v[114:117]
	v_mfma_f32_16x16x32_bf16 v[102:105], v[170:173], v[194:197], v[102:105]
	v_mfma_f32_16x16x32_bf16 v[98:101], v[178:181], v[194:197], v[98:101]
	v_mfma_f32_16x16x32_bf16 v[86:89], v[170:173], v[202:205], v[86:89]
	v_mfma_f32_16x16x32_bf16 v[82:85], v[178:181], v[202:205], v[82:85]
	v_mfma_f32_16x16x32_bf16 v[70:73], v[170:173], v[210:213], v[70:73]
	v_mfma_f32_16x16x32_bf16 v[66:69], v[178:181], v[210:213], v[66:69]
	s_setprio 0
	s_barrier
; #define PG8_STAGE(bufoff, gbase, voff) do { _Pragma("unroll") for (int _i = 0; _i < 2; ++_i) \
;         __builtin_amdgcn_global_load_lds((const unsigned*)((const char*)(gbase) + (voff)[_i]), (PG8_LAS unsigned*)(lds + (bufoff) + ldsw + _i * 8192), 16, 0, 0); } while (0)
; #define PG8_WAIT_V(n) asm volatile("s_waitcnt vmcnt(" #n ")" ::: "memory")
; #define PG8_WAIT_L(n) asm volatile("s_waitcnt lgkmcnt(" #n ")" ::: "memory")
; template <class Epi, class Sched, bool ALIGN_EPI = false, bool SP2 = false, bool GATHER = false>
; __device__ __forceinline__ void gemm_phase(PG8_LAS unsigned char* lds, const Gemm g, const Sched& S, const Epi& E, int tid_in, const int* rowsrc = nullptr, PG8_LAS int* idx_lds = nullptr) {
;     ...
;             PG8_LDA(At, 1, 1); PG8_STAGE(PG8_SB(1, 0), b3, voffB); PG8_STAGE(PG8_SB(1, 1), b3 + hstep, voffB); PG8_STAGE(PG8_SA(1, 0), a3, PG8_OS(0));
;             PG8_WAIT_V(8); PG8_WAIT_L(0); PG8_BAR; PG8_MMA(1, 0, At, B0); PG8_MMA(1, 1, At, B1); PG8_BAR; PG8_SCHED;
;             } else {
;             PG8_LDB(B0, 0, 0); PG8_SCHED; PG8_LDA(At, 0, 0); PG8_STAGE(PG8_SA(1, 1), a1 + hstepA, PG8_OA(1));
;             PG8_WAIT_L(8); PG8_BAR; PG8_WAIT_L(0); PG8_MMA(0, 0, At, B0); PG8_BAR; PG8_SCHED;
;             PG8_LDB(B1, 0, 1); PG8_STAGE(PG8_SB(0, 0), b2, voffB);
;             PG8_BAR; PG8_WAIT_L(0); PG8_MMA(0, 1, At, B1); PG8_BAR;
;             PG8_LDA(At, 0, 1); PG8_STAGE(PG8_SA(0, 0), a2, PG8_OS(0));
;             PG8_BAR; PG8_WAIT_L(0); PG8_MMA(1, 0, At, B0); PG8_BAR; PG8_SCHED;
;             PG8_STAGE(PG8_SB(0, 1), b2 + hstep, voffB);
;             PG8_WAIT_V(6); PG8_BAR; PG8_MMA(1, 1, At, B1); PG8_BAR;
;             PG8_LDB(B0, 1, 0); PG8_SCHED; PG8_LDA(At, 1, 0); PG8_STAGE(PG8_SA(0, 1), a2 + hstepA, PG8_OS(1));
;             PG8_WAIT_L(8); PG8_BAR; PG8_WAIT_L(0); PG8_MMA(0, 0, At, B0); PG8_BAR; PG8_SCHED;
;             PG8_LDB(B1, 1, 1); PG8_STAGE(PG8_SB(1, 0), b3, voffB);
;             PG8_BAR; PG8_WAIT_L(0); PG8_MMA(0, 1, At, B1); PG8_BAR;
;             PG8_LDA(At, 1, 1); PG8_STAGE(PG8_SA(1, 0), a3, PG8_OS(0));
;             PG8_BAR; PG8_WAIT_L(0); PG8_MMA(1, 0, At, B0); PG8_BAR; PG8_SCHED;
;             PG8_STAGE(PG8_SB(1, 1), b3 + hstep, voffB);
;             PG8_WAIT_V(6); PG8_BAR; PG8_MMA(1, 1, At, B1); PG8_BAR;
;             }
;         }
;         if constexpr (ALIGN_EPI) { if (wr == 0) PG8_BAR; }
	s_add_i32 s30, s58, s44
	v_lshl_add_u64 v[148:149], v[148:149], 0, s[10:11]
	s_mov_b32 m0, s30
	ds_read_b128 v[182:185], v153 offset:49152
	ds_read_b128 v[186:189], v153 offset:50176
	ds_read_b128 v[190:193], v153 offset:51200
	ds_read_b128 v[194:197], v153 offset:52224
	ds_read_b128 v[198:201], v153 offset:53248
	ds_read_b128 v[202:205], v153 offset:54272
	ds_read_b128 v[206:209], v153 offset:55296
	ds_read_b128 v[210:213], v153 offset:56320
	global_load_lds_dwordx4 v[148:149], off
	s_add_i32 m0, s30, 0x2000
	s_add_u32 s28, s28, 0x40080
	v_lshl_add_u64 v[148:149], v[214:215], 0, s[10:11]
	s_addc_u32 s29, s29, 0
	s_add_i32 s30, s59, s44
	global_load_lds_dwordx4 v[148:149], off
	v_lshl_add_u64 v[148:149], s[28:29], 0, v[134:135]
	s_mov_b32 m0, s30
	s_nop 0
	global_load_lds_dwordx4 v[148:149], off
	s_waitcnt vmcnt(5)
	s_waitcnt lgkmcnt(0)
	v_mfma_f32_16x16x32_bf16 v[62:65], v[142:145], v[182:185], v[62:65]
	v_mfma_f32_16x16x32_bf16 v[58:61], v[158:161], v[182:185], v[58:61]
	v_mfma_f32_16x16x32_bf16 v[46:49], v[142:145], v[190:193], v[46:49]
	s_barrier
	s_setprio 1
	s_waitcnt lgkmcnt(0)
	v_mfma_f32_16x16x32_bf16 v[42:45], v[158:161], v[190:193], v[42:45]
	v_mfma_f32_16x16x32_bf16 v[30:33], v[142:145], v[198:201], v[30:33]
	v_mfma_f32_16x16x32_bf16 v[26:29], v[158:161], v[198:201], v[26:29]
	v_mfma_f32_16x16x32_bf16 v[14:17], v[142:145], v[206:209], v[14:17]
	v_mfma_f32_16x16x32_bf16 v[10:13], v[158:161], v[206:209], v[10:13]
	v_lshl_add_u64 v[148:149], s[28:29], 0, v[130:131]
	s_add_i32 m0, s30, 0x2000
	s_nop 0
	global_load_lds_dwordx4 v[148:149], off
	v_mfma_f32_16x16x32_bf16 v[62:65], v[154:157], v[186:189], v[62:65]
	v_mfma_f32_16x16x32_bf16 v[58:61], v[162:165], v[186:189], v[58:61]
	v_mfma_f32_16x16x32_bf16 v[46:49], v[154:157], v[194:197], v[46:49]
	v_mfma_f32_16x16x32_bf16 v[42:45], v[162:165], v[194:197], v[42:45]
	v_mfma_f32_16x16x32_bf16 v[30:33], v[154:157], v[202:205], v[30:33]
	v_mfma_f32_16x16x32_bf16 v[26:29], v[162:165], v[202:205], v[26:29]
	v_mfma_f32_16x16x32_bf16 v[14:17], v[154:157], v[210:213], v[14:17]
	v_mfma_f32_16x16x32_bf16 v[10:13], v[162:165], v[210:213], v[10:13]
	v_lshl_add_u64 v[148:149], v[216:217], 0, s[10:11]
	s_mov_b32 m0, s51
	s_nop 0
	global_load_lds_dwordx4 v[148:149], off
	s_setprio 0
	s_setprio 1
	v_mfma_f32_16x16x32_bf16 v[54:57], v[166:169], v[182:185], v[54:57]
	v_mfma_f32_16x16x32_bf16 v[50:53], v[174:177], v[182:185], v[50:53]
	v_mfma_f32_16x16x32_bf16 v[38:41], v[166:169], v[190:193], v[38:41]
	v_mfma_f32_16x16x32_bf16 v[34:37], v[174:177], v[190:193], v[34:37]
	v_mfma_f32_16x16x32_bf16 v[22:25], v[166:169], v[198:201], v[22:25]
	v_mfma_f32_16x16x32_bf16 v[18:21], v[174:177], v[198:201], v[18:21]
	v_mfma_f32_16x16x32_bf16 v[6:9], v[166:169], v[206:209], v[6:9]
	v_mfma_f32_16x16x32_bf16 v[2:5], v[174:177], v[206:209], v[2:5]
	v_lshl_add_u64 v[148:149], v[218:219], 0, s[10:11]
	s_mov_b32 m0, s52
	s_nop 0
	global_load_lds_dwordx4 v[148:149], off
	v_mfma_f32_16x16x32_bf16 v[54:57], v[170:173], v[186:189], v[54:57]
	v_mfma_f32_16x16x32_bf16 v[50:53], v[178:181], v[186:189], v[50:53]
	v_mfma_f32_16x16x32_bf16 v[38:41], v[170:173], v[194:197], v[38:41]
	v_mfma_f32_16x16x32_bf16 v[34:37], v[178:181], v[194:197], v[34:37]
	v_mfma_f32_16x16x32_bf16 v[22:25], v[170:173], v[202:205], v[22:25]
	v_mfma_f32_16x16x32_bf16 v[18:21], v[178:181], v[202:205], v[18:21]
	v_mfma_f32_16x16x32_bf16 v[6:9], v[170:173], v[210:213], v[6:9]
	v_mfma_f32_16x16x32_bf16 v[2:5], v[178:181], v[210:213], v[2:5]
	s_setprio 0
	s_barrier
	s_add_i32 s57, s57, 2
	s_add_u32 s26, s26, 0x100
	s_addc_u32 s27, s27, 0
	s_add_u32 s55, s55, 0x100
	s_addc_u32 s56, s56, 0
	s_cmp_gt_u32 s57, 13
	s_cbranch_scc0 .LBB0_2005
	s_and_b64 vcc, exec, s[8:9]
	s_cbranch_vccz .LBB0_2008
	s_barrier
